# speedup vs baseline: 1.0018x; 1.0018x over previous
_Z11edge_kernelPKfPK15HIP_vector_typeIjLj4EES0_S0_S4_PfS5_:
	s_setprio 0
	s_load_dwordx8 s[64:71], s[0:1], 0x0
	s_load_dwordx4 s[72:75], s[0:1], 0x20
	s_load_dwordx2 s[76:77], s[0:1], 0x30
	s_waitcnt lgkmcnt(0)
	s_mov_b64 s[4:5], s[72:73]
	v_lshrrev_b32_e32 v192, 6, v0
	s_and_b32 s14, s2, 1
	s_lshr_b32 s3, s2, 6
	s_and_b32 s3, s3, 0x3fffff8
	v_lshl_or_b32 v1, s14, 2, v192
	v_or_b32_e32 v1, s3, v1
	v_lshlrev_b32_e32 v176, 4, v1
	v_mov_b32_e32 v177, 0
	v_and_b32_e32 v191, 63, v0
	v_lshlrev_b64 v[2:3], 10, v[176:177]
	s_waitcnt lgkmcnt(0)
	v_lshl_add_u64 v[2:3], s[4:5], 0, v[2:3]
	v_lshlrev_b32_e32 v176, 4, v191
	v_lshl_add_u64 v[184:185], v[2:3], 0, v[176:177]
	global_load_dwordx4 v[2:5], v[184:185], off
	s_mov_b64 s[4:5], 0x400
	v_lshl_add_u64 v[6:7], v[184:185], 0, s[4:5]
	global_load_dwordx4 v[170:173], v[6:7], off
	s_mov_b64 s[4:5], 0x800
	v_lshl_add_u64 v[6:7], v[184:185], 0, s[4:5]
	global_load_dwordx4 v[166:169], v[6:7], off
	s_mov_b64 s[4:5], 0xc00
	v_lshl_add_u64 v[6:7], v[184:185], 0, s[4:5]
	global_load_dwordx4 v[162:165], v[6:7], off
	s_mov_b64 s[4:5], 0x1000
	v_lshl_add_u64 v[6:7], v[184:185], 0, s[4:5]
	global_load_dwordx4 v[158:161], v[6:7], off
	s_mov_b64 s[4:5], 0x1400
	v_lshl_add_u64 v[6:7], v[184:185], 0, s[4:5]
	global_load_dwordx4 v[154:157], v[6:7], off
	s_mov_b64 s[4:5], 0x1800
	v_lshl_add_u64 v[6:7], v[184:185], 0, s[4:5]
	global_load_dwordx4 v[150:153], v[6:7], off
	s_mov_b64 s[4:5], 0x1c00
	v_lshl_add_u64 v[6:7], v[184:185], 0, s[4:5]
	global_load_dwordx4 v[146:149], v[6:7], off
	s_mov_b64 s[4:5], 0x2000
	v_lshl_add_u64 v[6:7], v[184:185], 0, s[4:5]
	global_load_dwordx4 v[110:113], v[6:7], off
	s_mov_b64 s[4:5], 0x2400
	v_lshl_add_u64 v[6:7], v[184:185], 0, s[4:5]
	global_load_dwordx4 v[90:93], v[6:7], off
	s_mov_b64 s[4:5], 0x2800
	v_lshl_add_u64 v[6:7], v[184:185], 0, s[4:5]
	global_load_dwordx4 v[86:89], v[6:7], off
	s_mov_b64 s[4:5], 0x2c00
	v_lshl_add_u64 v[6:7], v[184:185], 0, s[4:5]
	global_load_dwordx4 v[82:85], v[6:7], off
	v_cmp_lt_u32_e32 vcc, 63, v0
	s_and_saveexec_b64 s[4:5], vcc
	s_xor_b64 s[4:5], exec, s[4:5]
	s_cbranch_execz .LBB1_10
	s_mov_b64 s[6:7], s[68:69]
	v_cmp_lt_i32_e32 vcc, 1, v192
	s_and_saveexec_b64 s[8:9], vcc
	s_xor_b64 s[8:9], exec, s[8:9]
	s_cbranch_execz .LBB1_5
	v_cmp_eq_u32_e32 vcc, 2, v192
	s_and_saveexec_b64 s[10:11], vcc
	s_cbranch_execz .LBB1_4
	s_mov_b64 s[12:13], src_shared_base
	v_mov_b32_e32 v177, 0
	s_mov_b32 s12, 0xe800
	s_waitcnt lgkmcnt(0)
	v_lshl_add_u64 v[6:7], s[6:7], 0, v[176:177]
	s_mov_b64 s[16:17], 0x400
	s_cmp_lg_u64 s[12:13], 0
	v_lshl_add_u64 v[6:7], v[6:7], 0, s[16:17]
	s_cselect_b32 m0, 0xe800, -1
	s_nop 0
	global_load_lds_dwordx4 v[6:7], off

.Ledge_nosum:
	s_waitcnt lgkmcnt(0)
	s_barrier
	s_setprio 1
	ds_read_b128 v[6:9], v176
	ds_read_b128 v[10:13], v176 offset:1024
	ds_read_b128 v[14:17], v176 offset:2048
	ds_read_b128 v[194:197], v176 offset:3072
	ds_read_b128 v[198:201], v189 offset:57344
	ds_read_b128 v[18:21], v189 offset:57360
	ds_read_b128 v[202:205], v176 offset:4096
	ds_read_b128 v[206:209], v176 offset:5120
	ds_read_b128 v[210:213], v176 offset:6144
	ds_read_b128 v[214:217], v176 offset:7168
	ds_read_b128 v[218:221], v189 offset:57408
	ds_read_b128 v[222:225], v189 offset:57424
	s_movk_i32 s0, 0x1200
	v_and_b32_e32 v188, 31, v0
	v_lshlrev_b32_e32 v226, 16, v2
	v_and_b32_e32 v227, 0xffff0000, v2
	v_lshlrev_b32_e32 v22, 16, v3
	v_and_b32_e32 v23, 0xffff0000, v3
	v_lshlrev_b32_e32 v2, 16, v4
	v_and_b32_e32 v3, 0xffff0000, v4
	v_lshlrev_b32_e32 v4, 16, v5
	v_and_b32_e32 v5, 0xffff0000, v5
	s_waitcnt lgkmcnt(0)
	v_pk_mul_f32 v[228:229], v[18:19], v[2:3]
	v_pk_mul_f32 v[18:19], v[20:21], v[4:5]
	v_pk_mul_f32 v[24:25], v[200:201], v[22:23]
	v_pk_mul_f32 v[26:27], v[198:199], v[226:227]
	v_cvt_pk_bf16_f32 v4, v228, v229
	v_pk_fma_f32 v[246:247], v[200:201], v[22:23], v[18:19]
	v_pk_fma_f32 v[248:249], v[198:199], v[226:227], v[228:229]
	ds_read_b128 v[198:201], v176 offset:8192
	ds_read_b128 v[226:229], v176 offset:9216
	ds_read_b128 v[230:233], v176 offset:10240
	ds_read_b128 v[234:237], v176 offset:11264
	ds_read_b128 v[238:241], v189 offset:57472
	ds_read_b128 v[242:245], v189 offset:57488
	v_cvt_pk_bf16_f32 v2, v26, v27
	v_cvt_pk_bf16_f32 v5, v18, v19
	v_cvt_pk_bf16_f32 v3, v24, v25
	s_nop 1
	v_mfma_f32_32x32x16_bf16 v[50:65], v[6:9], v[2:5], 0
	v_mfma_f32_32x32x16_bf16 v[34:49], v[10:13], v[2:5], 0
	v_mfma_f32_32x32x16_bf16 v[18:33], v[14:17], v[2:5], 0
	v_mfma_f32_32x32x16_bf16 v[2:17], v[194:197], v[2:5], 0
	v_lshlrev_b32_e32 v194, 16, v172
	v_and_b32_e32 v195, 0xffff0000, v172
	v_lshlrev_b32_e32 v172, 16, v173
	v_and_b32_e32 v173, 0xffff0000, v173
	v_lshlrev_b32_e32 v250, 16, v170
	v_and_b32_e32 v251, 0xffff0000, v170
	v_lshlrev_b32_e32 v170, 16, v171
	v_and_b32_e32 v171, 0xffff0000, v171
	v_pk_mul_f32 v[222:223], v[222:223], v[194:195]
	v_pk_mul_f32 v[172:173], v[224:225], v[172:173]
	v_pk_mul_f32 v[252:253], v[220:221], v[170:171]
	v_pk_mul_f32 v[254:255], v[218:219], v[250:251]
	v_cvt_pk_bf16_f32 v197, v172, v173
	v_pk_fma_f32 v[170:171], v[220:221], v[170:171], v[172:173]
	v_pk_fma_f32 v[172:173], v[218:219], v[250:251], v[222:223]
	v_cvt_pk_bf16_f32 v196, v222, v223
	v_cvt_pk_bf16_f32 v194, v254, v255
	v_cvt_pk_bf16_f32 v195, v252, v253
	v_pk_add_f32 v[172:173], v[248:249], v[172:173]
	v_pk_add_f32 v[170:171], v[246:247], v[170:171]
	v_mfma_f32_32x32x16_bf16 v[50:65], v[202:205], v[194:197], v[50:65]
	v_pk_mov_b32 v[202:203], v[172:173], v[170:171] op_sel:[1,0]
	v_mov_b32_e32 v173, v171
	v_pk_add_f32 v[170:171], v[202:203], v[172:173]
	s_nop 0
	v_pk_add_f32 v[170:171], v[170:171], v[170:171] op_sel:[0,1] op_sel_hi:[1,0]
	v_mfma_f32_32x32x16_bf16 v[34:49], v[206:209], v[194:197], v[34:49]
	v_mfma_f32_32x32x16_bf16 v[18:33], v[210:213], v[194:197], v[18:33]
	ds_read_b128 v[202:205], v176 offset:12288
	ds_read_b128 v[206:209], v176 offset:13312
	ds_read_b128 v[210:213], v176 offset:14336
	ds_read_b128 v[218:221], v176 offset:15360
	ds_read_b128 v[222:225], v189 offset:57536
	ds_read_b128 v[246:249], v189 offset:57552
	v_mfma_f32_32x32x16_bf16 v[2:17], v[214:217], v[194:197], v[2:17]
	v_lshlrev_b32_e32 v172, 16, v166
	v_and_b32_e32 v173, 0xffff0000, v166
	v_lshlrev_b32_e32 v194, 16, v167
	v_and_b32_e32 v195, 0xffff0000, v167
	v_lshlrev_b32_e32 v166, 16, v168
	v_and_b32_e32 v167, 0xffff0000, v168
	v_lshlrev_b32_e32 v168, 16, v169
	v_and_b32_e32 v169, 0xffff0000, v169
	s_waitcnt lgkmcnt(0)
	v_pk_mul_f32 v[196:197], v[240:241], v[194:195]
	v_pk_mul_f32 v[214:215], v[238:239], v[172:173]
	v_pk_mul_f32 v[216:217], v[242:243], v[166:167]
	v_pk_mul_f32 v[242:243], v[244:245], v[168:169]
	v_cvt_pk_bf16_f32 v168, v216, v217
	v_cvt_pk_bf16_f32 v166, v214, v215
	v_cvt_pk_bf16_f32 v169, v242, v243
	v_cvt_pk_bf16_f32 v167, v196, v197
	v_pk_fma_f32 v[194:195], v[240:241], v[194:195], v[242:243]
	v_pk_fma_f32 v[172:173], v[238:239], v[172:173], v[216:217]
	v_mfma_f32_32x32x16_bf16 v[50:65], v[198:201], v[166:169], v[50:65]
	v_mfma_f32_32x32x16_bf16 v[34:49], v[226:229], v[166:169], v[34:49]
	v_mfma_f32_32x32x16_bf16 v[18:33], v[230:233], v[166:169], v[18:33]
	v_mfma_f32_32x32x16_bf16 v[2:17], v[234:237], v[166:169], v[2:17]
	v_lshlrev_b32_e32 v166, 16, v164
	v_and_b32_e32 v167, 0xffff0000, v164
	v_lshlrev_b32_e32 v164, 16, v165
	v_and_b32_e32 v165, 0xffff0000, v165
	v_mul_f32_e64 v216, v248, v164
	v_mul_f32_e64 v217, v249, v165
	v_mul_u32_u24_e32 v164, 0x140, v192
	v_lshlrev_b32_e32 v164, 4, v164
	v_mov_b32_e32 v165, v175
	v_mul_u32_u24_e32 v171, 0x1400, v192
	v_lshl_add_u64 v[164:165], s[10:11], 0, v[164:165]
	v_readfirstlane_b32 s2, v171
	v_lshlrev_b32_e32 v196, 16, v162
	v_and_b32_e32 v197, 0xffff0000, v162
	v_lshlrev_b32_e32 v162, 16, v163
	v_and_b32_e32 v163, 0xffff0000, v163
	v_lshl_add_u64 v[164:165], v[164:165], 0, v[176:177]
	s_movk_i32 s1, 0x1400
	s_mov_b32 m0, s2
	v_mov_b32_e32 v171, 0x1000
	v_pk_mul_f32 v[198:199], v[224:225], v[162:163]
	s_waitcnt lgkmcnt(0)
	s_barrier
	global_load_lds_dwordx4 v[164:165], off
	global_load_lds_dwordx4 v[164:165], off offset:1024
	global_load_lds_dwordx4 v[164:165], off offset:2048
	global_load_lds_dwordx4 v[164:165], off offset:3072
	s_mov_b64 s[2:3], 0x1000
	v_mad_u32_u24 v171, v192, s1, v171
	v_pk_mul_f32 v[214:215], v[246:247], v[166:167]
	v_cvt_pk_bf16_f32 v167, v198, v199
	v_lshl_add_u64 v[198:199], v[164:165], 0, s[2:3]
	v_readfirstlane_b32 s2, v171
	s_mov_b32 m0, s2
	v_pk_mul_f32 v[200:201], v[222:223], v[196:197]
	global_load_lds_dwordx4 v[198:199], off
	v_pk_fma_f32 v[162:163], v[224:225], v[162:163], v[216:217]
	v_pk_fma_f32 v[196:197], v[222:223], v[196:197], v[214:215]
	v_pk_add_f32 v[162:163], v[194:195], v[162:163]
	v_pk_add_f32 v[172:173], v[172:173], v[196:197]
	v_cvt_pk_bf16_f32 v168, v214, v215
	v_cvt_pk_bf16_f32 v166, v200, v201
	v_cvt_pk_bf16_f32 v169, v216, v217
	v_pk_mov_b32 v[194:195], v[172:173], v[162:163] op_sel:[1,0]
	v_mov_b32_e32 v173, v163
	v_mfma_f32_32x32x16_bf16 v[50:65], v[202:205], v[166:169], v[50:65]
	v_add_f32_e64 v162, v194, v172
	v_add_f32_e64 v163, v195, v173
	v_pk_add_f32 v[162:163], v[162:163], v[162:163] op_sel:[0,1] op_sel_hi:[1,0]
	v_mfma_f32_32x32x16_bf16 v[34:49], v[206:209], v[166:169], v[34:49]
	v_mfma_f32_32x32x16_bf16 v[18:33], v[210:213], v[166:169], v[18:33]
	ds_read_b128 v[194:197], v176 offset:20480
	ds_read_b128 v[198:201], v176 offset:21504
	ds_read_b128 v[202:205], v176 offset:22528
	ds_read_b128 v[206:209], v176 offset:23552
	ds_read_b128 v[210:213], v189 offset:57600
	ds_read_b128 v[214:217], v189 offset:57616
	ds_read_b128 v[222:225], v176 offset:24576
	ds_read_b128 v[226:229], v176 offset:25600
	ds_read_b128 v[230:233], v176 offset:26624
	ds_read_b128 v[234:237], v176 offset:27648
	ds_read_b128 v[238:241], v189 offset:57664
	ds_read_b128 v[242:245], v189 offset:57680
	v_mfma_f32_32x32x16_bf16 v[2:17], v[218:221], v[166:169], v[2:17]
	v_lshlrev_b32_e32 v166, 16, v158
	v_and_b32_e32 v167, 0xffff0000, v158
	v_lshlrev_b32_e32 v168, 16, v159
	v_and_b32_e32 v169, 0xffff0000, v159
	v_lshlrev_b32_e32 v158, 16, v160
	v_and_b32_e32 v159, 0xffff0000, v160
	v_lshlrev_b32_e32 v160, 16, v161
	v_and_b32_e32 v161, 0xffff0000, v161
	s_waitcnt lgkmcnt(0)
	v_pk_mul_f32 v[172:173], v[212:213], v[168:169]
	v_pk_mul_f32 v[218:219], v[210:211], v[166:167]
	v_pk_mul_f32 v[214:215], v[214:215], v[158:159]
	v_pk_mul_f32 v[216:217], v[216:217], v[160:161]
	v_cvt_pk_bf16_f32 v160, v214, v215
	v_cvt_pk_bf16_f32 v158, v218, v219
	v_cvt_pk_bf16_f32 v161, v216, v217
	v_cvt_pk_bf16_f32 v159, v172, v173
	v_pk_fma_f32 v[172:173], v[212:213], v[168:169], v[216:217]
	v_pk_fma_f32 v[218:219], v[210:211], v[166:167], v[214:215]
	v_mfma_f32_32x32x16_bf16 v[50:65], v[194:197], v[158:161], v[50:65]
	v_mfma_f32_32x32x16_bf16 v[34:49], v[198:201], v[158:161], v[34:49]
	v_mfma_f32_32x32x16_bf16 v[18:33], v[202:205], v[158:161], v[18:33]
	ds_read_b128 v[166:169], v176 offset:28672
	ds_read_b128 v[194:197], v176 offset:29696
	ds_read_b128 v[198:201], v176 offset:30720
	ds_read_b128 v[202:205], v176 offset:31744
	ds_read_b128 v[210:213], v189 offset:57728
	ds_read_b128 v[214:217], v189 offset:57744
	v_mfma_f32_32x32x16_bf16 v[2:17], v[206:209], v[158:161], v[2:17]
	v_lshlrev_b32_e32 v206, 16, v154
	v_and_b32_e32 v207, 0xffff0000, v154
	v_lshlrev_b32_e32 v154, 16, v155
	v_and_b32_e32 v155, 0xffff0000, v155
	v_lshlrev_b32_e32 v158, 16, v156
	v_and_b32_e32 v159, 0xffff0000, v156
	v_lshlrev_b32_e32 v156, 16, v157
	v_and_b32_e32 v157, 0xffff0000, v157
	v_pk_mul_f32 v[208:209], v[240:241], v[154:155]
	v_pk_mul_f32 v[220:221], v[238:239], v[206:207]
	v_pk_mul_f32 v[242:243], v[242:243], v[158:159]
	v_pk_mul_f32 v[156:157], v[244:245], v[156:157]
	v_cvt_pk_bf16_f32 v160, v242, v243
	v_cvt_pk_bf16_f32 v158, v220, v221
	v_cvt_pk_bf16_f32 v161, v156, v157
	v_cvt_pk_bf16_f32 v159, v208, v209
	v_pk_fma_f32 v[154:155], v[240:241], v[154:155], v[156:157]
	v_pk_fma_f32 v[156:157], v[238:239], v[206:207], v[242:243]
	v_mfma_f32_32x32x16_bf16 v[50:65], v[222:225], v[158:161], v[50:65]
	v_add_f32_e64 v156, v218, v156
	v_add_f32_e64 v157, v219, v157
	v_add_f32_e64 v154, v172, v154
	v_add_f32_e64 v155, v173, v155
	v_pk_mov_b32 v[172:173], v[156:157], v[154:155] op_sel:[1,0]
	v_mov_b32_e32 v157, v155
	v_pk_add_f32 v[154:155], v[172:173], v[156:157]
	v_mfma_f32_32x32x16_bf16 v[34:49], v[226:229], v[158:161], v[34:49]
	v_add_f32_e64 v156, v154, v155
	v_add_f32_e64 v157, v155, v154
	v_mfma_f32_32x32x16_bf16 v[18:33], v[230:233], v[158:161], v[18:33]
	ds_read_b128 v[206:209], v176 offset:32768
	ds_read_b128 v[218:221], v176 offset:33792
	ds_read_b128 v[222:225], v176 offset:34816
	ds_read_b128 v[226:229], v176 offset:35840
	ds_read_b128 v[230:233], v189 offset:57792
	ds_read_b128 v[238:241], v189 offset:57808
	v_mfma_f32_32x32x16_bf16 v[2:17], v[234:237], v[158:161], v[2:17]
	v_lshlrev_b32_e32 v154, 16, v150
	v_and_b32_e32 v155, 0xffff0000, v150
	v_lshlrev_b32_e32 v158, 16, v151
	v_and_b32_e32 v159, 0xffff0000, v151
	v_lshlrev_b32_e32 v150, 16, v152
	v_and_b32_e32 v151, 0xffff0000, v152
	v_lshlrev_b32_e32 v152, 16, v153
	v_and_b32_e32 v153, 0xffff0000, v153
	s_waitcnt lgkmcnt(0)
	v_pk_mul_f32 v[160:161], v[212:213], v[158:159]
	v_pk_mul_f32 v[172:173], v[210:211], v[154:155]
	v_pk_mul_f32 v[214:215], v[214:215], v[150:151]
	v_pk_mul_f32 v[216:217], v[216:217], v[152:153]
	v_cvt_pk_bf16_f32 v152, v214, v215
	v_cvt_pk_bf16_f32 v150, v172, v173
	v_cvt_pk_bf16_f32 v153, v216, v217
	v_cvt_pk_bf16_f32 v151, v160, v161
	v_pk_fma_f32 v[158:159], v[212:213], v[158:159], v[216:217]
	v_pk_fma_f32 v[154:155], v[210:211], v[154:155], v[214:215]
	v_mfma_f32_32x32x16_bf16 v[50:65], v[166:169], v[150:153], v[50:65]
	v_mfma_f32_32x32x16_bf16 v[34:49], v[194:197], v[150:153], v[34:49]
	v_mfma_f32_32x32x16_bf16 v[18:33], v[198:201], v[150:153], v[18:33]
	v_mfma_f32_32x32x16_bf16 v[2:17], v[202:205], v[150:153], v[2:17]
	v_lshlrev_b32_e32 v152, 16, v146
	v_and_b32_e32 v153, 0xffff0000, v146
	v_lshlrev_b32_e32 v146, 16, v147
	v_and_b32_e32 v147, 0xffff0000, v147
	v_mov_b32_e32 v157, 0x5000
	v_lshlrev_b32_e32 v150, 16, v148
	v_and_b32_e32 v151, 0xffff0000, v148
	v_lshlrev_b32_e32 v148, 16, v149
	v_and_b32_e32 v149, 0xffff0000, v149
	v_pk_mul_f32 v[160:161], v[232:233], v[146:147]
	s_mov_b64 s[2:3], 0x5000
	v_mad_u32_u24 v157, v192, s1, v157
	v_pk_mul_f32 v[172:173], v[240:241], v[148:149]
	v_cvt_pk_bf16_f32 v149, v160, v161
	v_lshl_add_u64 v[160:161], v[164:165], 0, s[2:3]
	v_readfirstlane_b32 s2, v157
	s_mov_b32 m0, s2
	v_mov_b32_e32 v157, 0x6000
	s_waitcnt lgkmcnt(0)
	s_barrier
	global_load_lds_dwordx4 v[160:161], off
	global_load_lds_dwordx4 v[160:161], off offset:1024
	global_load_lds_dwordx4 v[160:161], off offset:2048
	global_load_lds_dwordx4 v[160:161], off offset:3072
	v_mad_u32_u24 v157, v192, s1, v157
	s_mov_b64 s[2:3], 0x6000
	v_readfirstlane_b32 s1, v157
	v_lshl_add_u64 v[160:161], v[164:165], 0, s[2:3]
	s_mov_b32 m0, s1
	v_pk_mul_f32 v[168:169], v[238:239], v[150:151]
	global_load_lds_dwordx4 v[160:161], off
	v_pk_mul_f32 v[166:167], v[230:231], v[152:153]
	v_pk_fma_f32 v[146:147], v[232:233], v[146:147], v[172:173]
	v_pk_fma_f32 v[152:153], v[230:231], v[152:153], v[168:169]
	v_pk_add_f32 v[146:147], v[158:159], v[146:147]
	v_pk_add_f32 v[152:153], v[154:155], v[152:153]
	v_cvt_pk_bf16_f32 v150, v168, v169
	v_cvt_pk_bf16_f32 v148, v166, v167
	v_cvt_pk_bf16_f32 v151, v172, v173
	v_pk_mov_b32 v[154:155], v[152:153], v[146:147] op_sel:[1,0]
	v_mov_b32_e32 v153, v147
	v_mfma_f32_32x32x16_bf16 v[50:65], v[206:209], v[148:151], v[50:65]
	v_add_f32_e64 v146, v154, v152
	v_add_f32_e64 v147, v155, v153
	v_pk_add_f32 v[146:147], v[146:147], v[146:147] op_sel:[0,1] op_sel_hi:[1,0]
	v_mfma_f32_32x32x16_bf16 v[34:49], v[218:221], v[148:151], v[34:49]
	v_mfma_f32_32x32x16_bf16 v[18:33], v[222:225], v[148:151], v[18:33]
	ds_read_b128 v[152:155], v176 offset:40960
	ds_read_b128 v[158:161], v176 offset:41984
	ds_read_b128 v[164:167], v176 offset:43008
	ds_read_b128 v[194:197], v176 offset:44032
	ds_read_b128 v[198:201], v189 offset:57856
	ds_read_b128 v[202:205], v189 offset:57872
	ds_read_b128 v[206:209], v176 offset:45056
	ds_read_b128 v[210:213], v176 offset:46080
	ds_read_b128 v[214:217], v176 offset:47104
	ds_read_b128 v[218:221], v176 offset:48128
	ds_read_b128 v[222:225], v189 offset:57920
	ds_read_b128 v[230:233], v189 offset:57936
	v_mfma_f32_32x32x16_bf16 v[2:17], v[226:229], v[148:151], v[2:17]
	v_lshlrev_b32_e32 v148, 16, v110
	v_and_b32_e32 v149, 0xffff0000, v110
	v_lshlrev_b32_e32 v150, 16, v111
	v_and_b32_e32 v151, 0xffff0000, v111
	v_lshlrev_b32_e32 v110, 16, v112
	v_and_b32_e32 v111, 0xffff0000, v112
	v_lshlrev_b32_e32 v112, 16, v113
	v_and_b32_e32 v113, 0xffff0000, v113
	s_waitcnt lgkmcnt(0)
	v_pk_mul_f32 v[168:169], v[200:201], v[150:151]
	v_pk_mul_f32 v[172:173], v[198:199], v[148:149]
	v_pk_mul_f32 v[202:203], v[202:203], v[110:111]
	v_pk_mul_f32 v[204:205], v[204:205], v[112:113]
	v_cvt_pk_bf16_f32 v112, v202, v203
	v_cvt_pk_bf16_f32 v110, v172, v173
	v_cvt_pk_bf16_f32 v113, v204, v205
	v_cvt_pk_bf16_f32 v111, v168, v169
	v_pk_fma_f32 v[148:149], v[198:199], v[148:149], v[202:203]
	s_nop 0
	v_mfma_f32_32x32x16_bf16 v[50:65], v[152:155], v[110:113], v[50:65]
	v_fma_f32 v154, v200, v150, v204
	v_fma_f32 v155, v201, v151, v205
	v_mfma_f32_32x32x16_bf16 v[34:49], v[158:161], v[110:113], v[34:49]
	v_mfma_f32_32x32x16_bf16 v[18:33], v[164:167], v[110:113], v[18:33]
	ds_read_b128 v[150:153], v176 offset:49152
	ds_read_b128 v[158:161], v176 offset:50176
	ds_read_b128 v[164:167], v176 offset:51200
	ds_read_b128 v[198:201], v176 offset:52224
	ds_read_b128 v[202:205], v189 offset:57984
	ds_read_b128 v[226:229], v189 offset:58000
	v_mfma_f32_32x32x16_bf16 v[2:17], v[194:197], v[110:113], v[2:17]
	v_lshlrev_b32_e32 v110, 16, v90
	v_and_b32_e32 v111, 0xffff0000, v90
	v_lshlrev_b32_e32 v112, 16, v91
	v_and_b32_e32 v113, 0xffff0000, v91
	v_lshlrev_b32_e32 v90, 16, v92
	v_and_b32_e32 v91, 0xffff0000, v92
	v_lshlrev_b32_e32 v92, 16, v93
	v_and_b32_e32 v93, 0xffff0000, v93
	v_pk_mul_f32 v[194:195], v[230:231], v[90:91]
	v_pk_mul_f32 v[196:197], v[232:233], v[92:93]
	v_pk_mul_f32 v[168:169], v[224:225], v[112:113]
	v_pk_mul_f32 v[172:173], v[222:223], v[110:111]
	v_pk_fma_f32 v[112:113], v[224:225], v[112:113], v[196:197]
	v_pk_fma_f32 v[110:111], v[222:223], v[110:111], v[194:195]
	v_pk_add_f32 v[112:113], v[154:155], v[112:113]
	v_pk_add_f32 v[110:111], v[148:149], v[110:111]
	v_cvt_pk_bf16_f32 v92, v194, v195
	v_pk_mov_b32 v[148:149], v[110:111], v[112:113] op_sel:[1,0]
	v_mov_b32_e32 v111, v113
	v_cvt_pk_bf16_f32 v90, v172, v173
	v_cvt_pk_bf16_f32 v93, v196, v197
	v_cvt_pk_bf16_f32 v91, v168, v169
	v_pk_add_f32 v[110:111], v[148:149], v[110:111]
	s_nop 0
	v_mfma_f32_32x32x16_bf16 v[50:65], v[206:209], v[90:93], v[50:65]
	v_add_f32_e64 v148, v110, v111
	v_add_f32_e64 v149, v111, v110
	v_mfma_f32_32x32x16_bf16 v[34:49], v[210:213], v[90:93], v[34:49]
	v_mfma_f32_32x32x16_bf16 v[18:33], v[214:217], v[90:93], v[18:33]
	ds_read_b128 v[110:113], v176 offset:53248
	ds_read_b128 v[194:197], v176 offset:54272
	ds_read_b128 v[206:209], v176 offset:55296
	ds_read_b128 v[210:213], v176 offset:56320
	ds_read_b128 v[214:217], v189 offset:58048
	ds_read_b128 v[222:225], v189 offset:58064
	v_mfma_f32_32x32x16_bf16 v[2:17], v[218:221], v[90:93], v[2:17]
	v_lshlrev_b32_e32 v90, 16, v86
	v_and_b32_e32 v91, 0xffff0000, v86
	v_lshlrev_b32_e32 v92, 16, v87
	v_and_b32_e32 v93, 0xffff0000, v87
	v_lshlrev_b32_e32 v86, 16, v88
	v_and_b32_e32 v87, 0xffff0000, v88
	v_lshlrev_b32_e32 v88, 16, v89
	v_and_b32_e32 v89, 0xffff0000, v89
	s_waitcnt lgkmcnt(0)
	v_pk_mul_f32 v[154:155], v[204:205], v[92:93]
	v_pk_mul_f32 v[168:169], v[202:203], v[90:91]
	v_pk_mul_f32 v[172:173], v[226:227], v[86:87]
	v_pk_mul_f32 v[218:219], v[228:229], v[88:89]
	v_cvt_pk_bf16_f32 v88, v172, v173
	v_cvt_pk_bf16_f32 v86, v168, v169
	v_cvt_pk_bf16_f32 v89, v218, v219
	v_cvt_pk_bf16_f32 v87, v154, v155
	v_pk_fma_f32 v[92:93], v[204:205], v[92:93], v[218:219]
	v_pk_fma_f32 v[90:91], v[202:203], v[90:91], v[172:173]
	v_mfma_f32_32x32x16_bf16 v[50:65], v[150:153], v[86:89], v[50:65]
	v_mfma_f32_32x32x16_bf16 v[34:49], v[158:161], v[86:89], v[34:49]
	v_mfma_f32_32x32x16_bf16 v[18:33], v[164:167], v[86:89], v[18:33]
	v_mfma_f32_32x32x16_bf16 v[2:17], v[198:201], v[86:89], v[2:17]
	v_lshlrev_b32_e32 v86, 16, v82
	v_and_b32_e32 v87, 0xffff0000, v82
	v_lshlrev_b32_e32 v88, 16, v83
	v_and_b32_e32 v89, 0xffff0000, v83
	v_lshlrev_b32_e32 v82, 16, v84
	v_and_b32_e32 v83, 0xffff0000, v84
	v_lshlrev_b32_e32 v84, 16, v85
	v_and_b32_e32 v85, 0xffff0000, v85
	v_pk_mul_f32 v[150:151], v[216:217], v[88:89]
	v_pk_mul_f32 v[152:153], v[214:215], v[86:87]
	v_pk_mul_f32 v[154:155], v[222:223], v[82:83]
	v_pk_mul_f32 v[158:159], v[224:225], v[84:85]
	v_cvt_pk_bf16_f32 v84, v154, v155
	v_cvt_pk_bf16_f32 v82, v152, v153
	v_cvt_pk_bf16_f32 v85, v158, v159
	v_cvt_pk_bf16_f32 v83, v150, v151
	v_pk_fma_f32 v[88:89], v[216:217], v[88:89], v[158:159]
	v_pk_fma_f32 v[86:87], v[214:215], v[86:87], v[154:155]
	s_mov_b64 s[2:3], 0x3000
	v_mfma_f32_32x32x16_bf16 v[50:65], v[110:113], v[82:85], v[50:65]
	v_add_f32_e64 v86, v90, v86
	v_add_f32_e64 v87, v91, v87
	v_add_f32_e64 v88, v92, v88
	v_add_f32_e64 v89, v93, v89
	s_waitcnt vmcnt(5)
	v_pk_mov_b32 v[90:91], v[86:87], v[88:89] op_sel:[1,0]
	v_mov_b32_e32 v87, v89
	v_pk_add_f32 v[86:87], v[90:91], v[86:87]
	v_lshrrev_b32_e32 v161, 3, v191
	v_mfma_f32_32x32x16_bf16 v[34:49], v[194:197], v[82:85], v[34:49]
	s_movk_i32 s1, 0x90
	v_or_b32_e32 v152, v1, v174
	v_add_f32_e64 v150, v86, v87
	v_add_f32_e64 v151, v87, v86
	v_mad_u32_u24 v155, v161, s1, v152
	v_mul_u32_u24_e32 v147, 0x90, v188
	v_mad_u32_u24 v149, v192, s0, v147
	v_and_b32_e32 v147, 32, v0
	v_mfma_f32_32x32x16_bf16 v[18:33], v[206:209], v[82:85], v[18:33]
	v_add_u32_e32 v151, v149, v147
	v_lshrrev_b32_e32 v147, 1, v191
	v_and_b32_e32 v154, 16, v147
	v_add_u32_e32 v160, v149, v154
	v_sub_u32_e32 v147, v189, v154
	s_mov_b64 s[8:9], 0x16000
	s_brev_b32 s0, 60
	v_mfma_f32_32x32x16_bf16 v[2:17], v[210:213], v[82:85], v[2:17]
	v_lshl_add_u64 v[82:83], v[184:185], 0, s[2:3]
	s_mov_b64 s[2:3], 0x3400
	global_load_dwordx4 v[110:113], v[82:83], off
	v_lshl_add_u64 v[82:83], v[184:185], 0, s[2:3]
	s_mov_b64 s[2:3], 0x3800
	global_load_dwordx4 v[90:93], v[82:83], off
	v_lshl_add_u64 v[82:83], v[184:185], 0, s[2:3]
	s_mov_b64 s[2:3], 0x3c00
	global_load_dwordx4 v[86:89], v[82:83], off
	v_lshl_add_u64 v[82:83], v[184:185], 0, s[2:3]
	global_load_dwordx4 v[82:85], v[82:83], off
	s_waitcnt lgkmcnt(0)
	s_barrier
	ds_write_b128 v155, v[142:145] offset:61440
	v_mov_b32_e32 v142, 0x480
	v_mad_u32_u24 v165, v161, s1, v142
	v_add_u32_e32 v157, v152, v165
	ds_write_b128 v157, v[134:137] offset:61440
	v_mov_b32_e32 v134, 0x900
	v_mad_u32_u24 v164, v161, s1, v134
	v_add_u32_e32 v171, v152, v164
	ds_write_b128 v171, v[130:133] offset:61440
	v_mov_b32_e32 v130, 0xd80
	v_mad_u32_u24 v163, v161, s1, v130
	v_add_u32_e32 v174, v152, v163
	ds_write_b128 v174, v[138:141] offset:61440
	ds_read_b128 v[142:145], v151 offset:61440
	ds_read_b128 v[138:141], v151 offset:61456
	ds_read_b128 v[134:137], v151 offset:61504
	ds_read_b128 v[130:133], v151 offset:61520
	ds_read_b128 v[166:169], v160 offset:61440
	ds_read_b128 v[192:195], v160 offset:61472
	ds_read_b128 v[196:199], v147 offset:58368
	ds_read_b128 v[200:203], v147 offset:58400
	ds_read_b128 v[204:207], v160 offset:61504
	ds_read_b128 v[208:211], v160 offset:61536
	ds_read_b128 v[212:215], v147 offset:58432
	ds_read_b128 v[216:219], v147 offset:58464
	s_waitcnt lgkmcnt(0)
	v_pk_add_f32 v[152:153], v[168:169], v[198:199]
	v_pk_add_f32 v[158:159], v[166:167], v[196:197]
	v_pk_add_f32 v[166:167], v[194:195], v[202:203]
	v_pk_add_f32 v[168:169], v[192:193], v[200:201]
	v_pk_add_f32 v[192:193], v[210:211], v[218:219]
	v_pk_add_f32 v[194:195], v[208:209], v[216:217]
	v_pk_add_f32 v[172:173], v[206:207], v[214:215]
	v_pk_add_f32 v[184:185], v[204:205], v[212:213]
	v_pk_add_f32 v[62:63], v[194:195], v[62:63]
	v_pk_add_f32 v[54:55], v[168:169], v[54:55]
	v_pk_add_f32 v[64:65], v[192:193], v[64:65]
	v_pk_add_f32 v[56:57], v[166:167], v[56:57]
	ds_write_b128 v155, v[114:117] offset:61440
	ds_write_b128 v157, v[118:121] offset:61440
	ds_write_b128 v171, v[122:125] offset:61440
	ds_write_b128 v174, v[126:129] offset:61440
	ds_read_b128 v[126:129], v151 offset:61440
	ds_read_b128 v[122:125], v151 offset:61456
	ds_read_b128 v[118:121], v151 offset:61504
	ds_read_b128 v[114:117], v151 offset:61520
	ds_read_b128 v[166:169], v160 offset:61440
	ds_read_b128 v[192:195], v160 offset:61472
	ds_read_b128 v[196:199], v147 offset:58496
	ds_read_b128 v[200:203], v147 offset:58528
	ds_read_b128 v[204:207], v160 offset:61504
	ds_read_b128 v[208:211], v160 offset:61536
	ds_read_b128 v[212:215], v147 offset:58560
	ds_read_b128 v[216:219], v147 offset:58592
	v_pk_add_f32 v[52:53], v[152:153], v[52:53]
	v_pk_add_f32 v[50:51], v[158:159], v[50:51]
	s_waitcnt lgkmcnt(0)
	v_pk_add_f32 v[152:153], v[168:169], v[198:199]
	v_pk_add_f32 v[158:159], v[166:167], v[196:197]
	v_pk_add_f32 v[166:167], v[194:195], v[202:203]
	v_pk_add_f32 v[168:169], v[192:193], v[200:201]
	v_pk_add_f32 v[192:193], v[210:211], v[218:219]
	v_pk_add_f32 v[194:195], v[208:209], v[216:217]
	v_pk_add_f32 v[58:59], v[184:185], v[58:59]
	v_pk_add_f32 v[60:61], v[172:173], v[60:61]
	v_pk_add_f32 v[172:173], v[206:207], v[214:215]
	v_pk_add_f32 v[184:185], v[204:205], v[212:213]
	v_pk_add_f32 v[46:47], v[194:195], v[46:47]
	v_pk_add_f32 v[38:39], v[168:169], v[38:39]
	v_pk_add_f32 v[48:49], v[192:193], v[48:49]
	v_pk_add_f32 v[40:41], v[166:167], v[40:41]
	ds_write_b128 v155, v[102:105] offset:61440
	ds_write_b128 v157, v[94:97] offset:61440
	ds_write_b128 v171, v[98:101] offset:61440
	ds_write_b128 v174, v[106:109] offset:61440
	ds_read_b128 v[106:109], v151 offset:61440
	ds_read_b128 v[102:105], v151 offset:61456
	ds_read_b128 v[98:101], v151 offset:61504
	ds_read_b128 v[94:97], v151 offset:61520
	ds_read_b128 v[166:169], v160 offset:61440
	ds_read_b128 v[192:195], v160 offset:61472
	ds_read_b128 v[196:199], v147 offset:58624
	ds_read_b128 v[200:203], v147 offset:58656
	ds_read_b128 v[204:207], v160 offset:61504
	ds_read_b128 v[208:211], v160 offset:61536
	ds_read_b128 v[212:215], v147 offset:58688
	ds_read_b128 v[216:219], v147 offset:58720
	v_pk_add_f32 v[36:37], v[152:153], v[36:37]
	v_pk_add_f32 v[34:35], v[158:159], v[34:35]
	s_waitcnt lgkmcnt(0)
	v_pk_add_f32 v[152:153], v[168:169], v[198:199]
	v_pk_add_f32 v[158:159], v[166:167], v[196:197]
	v_pk_add_f32 v[166:167], v[194:195], v[202:203]
	v_pk_add_f32 v[168:169], v[192:193], v[200:201]
	v_pk_add_f32 v[192:193], v[210:211], v[218:219]
	v_pk_add_f32 v[194:195], v[208:209], v[216:217]
	v_add_f32_e32 v149, 0, v142
	v_pk_add_f32 v[42:43], v[184:185], v[42:43]
	v_pk_add_f32 v[44:45], v[172:173], v[44:45]
	v_pk_add_f32 v[172:173], v[206:207], v[214:215]
	v_pk_add_f32 v[184:185], v[204:205], v[212:213]
	v_pk_add_f32 v[30:31], v[194:195], v[30:31]
	v_pk_add_f32 v[22:23], v[168:169], v[22:23]
	v_pk_add_f32 v[32:33], v[192:193], v[32:33]
	v_pk_add_f32 v[24:25], v[166:167], v[24:25]
	ds_write_b128 v155, v[66:69] offset:61440
	ds_write_b128 v157, v[70:73] offset:61440
	ds_write_b128 v171, v[74:77] offset:61440
	ds_write_b128 v174, v[78:81] offset:61440
	ds_read_b128 v[78:81], v151 offset:61440
	ds_read_b128 v[74:77], v151 offset:61456
	ds_read_b128 v[70:73], v151 offset:61504
	ds_read_b128 v[66:69], v151 offset:61520
	ds_read_b128 v[166:169], v160 offset:61440
	ds_read_b128 v[192:195], v160 offset:61472
	ds_read_b128 v[196:199], v147 offset:58752
	ds_read_b128 v[200:203], v147 offset:58784
	ds_read_b128 v[204:207], v160 offset:61504
	ds_read_b128 v[208:211], v160 offset:61536
	ds_read_b128 v[212:215], v147 offset:58816
	ds_read_b128 v[216:219], v147 offset:58848
	v_add_f32_e32 v149, v149, v143
	v_mul_f32_e32 v151, v143, v143
	v_fmac_f32_e32 v151, v142, v142
	v_add_f32_e32 v149, v149, v144
	v_fmac_f32_e32 v151, v144, v144
	v_add_f32_e32 v149, v149, v145
	v_fmac_f32_e32 v151, v145, v145
	v_add_f32_e32 v149, v149, v138
	v_fmac_f32_e32 v151, v138, v138
	v_add_f32_e32 v149, v149, v139
	v_fmac_f32_e32 v151, v139, v139
	v_add_f32_e32 v149, v149, v140
	v_fmac_f32_e32 v151, v140, v140
	v_add_f32_e32 v149, v149, v141
	v_fmac_f32_e32 v151, v141, v141
	v_add_f32_e32 v149, v149, v134
	v_fmac_f32_e32 v151, v134, v134
	v_add_f32_e32 v149, v149, v135
	v_fmac_f32_e32 v151, v135, v135
	v_add_f32_e32 v149, v149, v136
	v_fmac_f32_e32 v151, v136, v136
	v_add_f32_e32 v149, v149, v137
	v_fmac_f32_e32 v151, v137, v137
	v_add_f32_e32 v149, v149, v130
	v_fmac_f32_e32 v151, v130, v130
	v_add_f32_e32 v149, v149, v131
	v_fmac_f32_e32 v151, v131, v131
	v_add_f32_e32 v149, v149, v132
	v_fmac_f32_e32 v151, v132, v132
	v_add_f32_e32 v149, v149, v133
	v_fmac_f32_e32 v151, v133, v133
	v_add_f32_e32 v149, v149, v126
	v_fmac_f32_e32 v151, v126, v126
	v_add_f32_e32 v149, v149, v127
	v_fmac_f32_e32 v151, v127, v127
	v_add_f32_e32 v149, v149, v128
	v_fmac_f32_e32 v151, v128, v128
	v_add_f32_e32 v149, v149, v129
	v_fmac_f32_e32 v151, v129, v129
	v_add_f32_e32 v149, v149, v122
	v_fmac_f32_e32 v151, v122, v122
	v_add_f32_e32 v149, v149, v123
	v_fmac_f32_e32 v151, v123, v123
	v_add_f32_e32 v149, v149, v124
	v_fmac_f32_e32 v151, v124, v124
	v_add_f32_e32 v149, v149, v125
	v_fmac_f32_e32 v151, v125, v125
	v_add_f32_e32 v149, v149, v118
	v_fmac_f32_e32 v151, v118, v118
	v_add_f32_e32 v149, v149, v119
	v_fmac_f32_e32 v151, v119, v119
	v_add_f32_e32 v149, v149, v120
	v_fmac_f32_e32 v151, v120, v120
	v_add_f32_e32 v149, v149, v121
	v_fmac_f32_e32 v151, v121, v121
	v_add_f32_e32 v149, v149, v114
	v_fmac_f32_e32 v151, v114, v114
	v_add_f32_e32 v149, v149, v115
	v_fmac_f32_e32 v151, v115, v115
	v_add_f32_e32 v149, v149, v116
	v_fmac_f32_e32 v151, v116, v116
	v_add_f32_e32 v149, v149, v117
	v_fmac_f32_e32 v151, v117, v117
	v_add_f32_e32 v149, v149, v106
	v_fmac_f32_e32 v151, v106, v106
	v_add_f32_e32 v149, v149, v107
	v_fmac_f32_e32 v151, v107, v107
	v_add_f32_e32 v149, v149, v108
	v_fmac_f32_e32 v151, v108, v108
	v_add_f32_e32 v149, v149, v109
	v_fmac_f32_e32 v151, v109, v109
	v_add_f32_e32 v149, v149, v102
	v_fmac_f32_e32 v151, v102, v102
	v_add_f32_e32 v149, v149, v103
	v_fmac_f32_e32 v151, v103, v103
	v_add_f32_e32 v149, v149, v104
	v_fmac_f32_e32 v151, v104, v104
	v_add_f32_e32 v149, v149, v105
	v_fmac_f32_e32 v151, v105, v105
	v_add_f32_e32 v149, v149, v98
	v_fmac_f32_e32 v151, v98, v98
	v_add_f32_e32 v149, v149, v99
	v_fmac_f32_e32 v151, v99, v99
	v_add_f32_e32 v149, v149, v100
	v_fmac_f32_e32 v151, v100, v100
	v_add_f32_e32 v149, v149, v101
	v_fmac_f32_e32 v151, v101, v101
	v_add_f32_e32 v149, v149, v94
	v_fmac_f32_e32 v151, v94, v94
	v_add_f32_e32 v149, v149, v95
	v_fmac_f32_e32 v151, v95, v95
	v_add_f32_e32 v149, v149, v96
	v_fmac_f32_e32 v151, v96, v96
	v_add_f32_e32 v149, v149, v97
	v_fmac_f32_e32 v151, v97, v97
	s_waitcnt lgkmcnt(0)
	v_add_f32_e32 v149, v149, v78
	v_fmac_f32_e32 v151, v78, v78
	v_add_f32_e32 v149, v149, v79
	v_fmac_f32_e32 v151, v79, v79
	v_add_f32_e32 v149, v149, v80
	v_fmac_f32_e32 v151, v80, v80
	v_add_f32_e32 v149, v149, v81
	v_fmac_f32_e32 v151, v81, v81
	v_add_f32_e32 v149, v149, v74
	v_fmac_f32_e32 v151, v74, v74
	v_add_f32_e32 v149, v149, v75
	v_fmac_f32_e32 v151, v75, v75
	v_add_f32_e32 v149, v149, v76
	v_pk_add_f32 v[20:21], v[152:153], v[20:21]
	v_pk_add_f32 v[152:153], v[168:169], v[198:199]
	v_pk_add_f32 v[168:169], v[192:193], v[200:201]
	v_fmac_f32_e32 v151, v76, v76
	v_add_f32_e32 v149, v149, v77
	v_pk_add_f32 v[6:7], v[168:169], v[6:7]
	v_fmac_f32_e32 v151, v77, v77
	v_add_f32_e32 v149, v149, v70
	v_pk_mul_f32 v[168:169], v[70:71], v[70:71]
	v_pk_add_f32 v[18:19], v[158:159], v[18:19]
	v_pk_add_f32 v[158:159], v[166:167], v[196:197]
	v_pk_add_f32 v[166:167], v[194:195], v[202:203]
	v_add_f32_e32 v149, v149, v71
	v_add_f32_e32 v151, v151, v168
	v_pk_add_f32 v[8:9], v[166:167], v[8:9]
	v_pk_mul_f32 v[166:167], v[72:73], v[72:73]
	v_add_f32_e32 v151, v151, v169
	v_add_f32_e32 v149, v149, v72
	v_add_f32_e32 v149, v149, v73
	v_add_f32_e32 v151, v151, v166
	v_add_f32_e32 v151, v151, v167
	v_add_f32_e32 v149, v149, v66
	v_pk_mul_f32 v[168:169], v[66:67], v[66:67]
	v_add_f32_e32 v149, v149, v67
	v_add_f32_e32 v151, v151, v168
	v_pk_mul_f32 v[166:167], v[68:69], v[68:69]
	v_add_f32_e32 v151, v151, v169
	v_add_f32_e32 v149, v149, v68
	v_add_f32_e32 v169, v149, v69
	v_add_f32_e32 v149, v151, v166
	v_add_f32_e32 v168, v149, v167
	v_mov_b32_e32 v167, v169
	v_mov_b32_e32 v166, v168
	s_nop 0
	v_permlane32_swap_b32_e32 v169, v167
	v_permlane32_swap_b32_e32 v168, v166
	v_readfirstlane_b32 s3, v187
	v_pk_add_f32 v[166:167], v[168:169], v[166:167]
	v_lshl_add_u64 v[168:169], v[180:181], 0, s[8:9]
	s_mov_b32 m0, s3
	s_nop 0
	global_load_lds_dwordx4 v[168:169], off
	global_load_lds_dwordx4 v[168:169], off offset:1024
	global_load_lds_dwordx4 v[168:169], off offset:2048
	global_load_lds_dwordx4 v[168:169], off offset:3072
	v_pk_mul_f32 v[166:167], v[166:167], s[0:1] op_sel_hi:[1,0]
	s_mov_b32 s2, 0x800000
	v_fma_f32 v149, -v167, v167, v166
	v_add_f32_e32 v149, 0x3727c5ac, v149
	v_mul_f32_e32 v151, 0x4b800000, v149
	v_cmp_gt_f32_e32 vcc, s2, v149
	v_pk_add_f32 v[4:5], v[152:153], v[4:5]
	v_pk_add_f32 v[2:3], v[158:159], v[2:3]
	v_cndmask_b32_e32 v149, v149, v151, vcc
	v_rsq_f32_e32 v149, v149
	v_pk_add_f32 v[26:27], v[184:185], v[26:27]
	v_pk_add_f32 v[28:29], v[172:173], v[28:29]
	v_pk_add_f32 v[172:173], v[206:207], v[214:215]
	v_mul_f32_e32 v151, 0x45800000, v149
	v_cndmask_b32_e32 v152, v149, v151, vcc
	v_mul_f32_e64 v158, v152, -v167
	v_pk_add_f32 v[184:185], v[204:205], v[212:213]
	v_pk_add_f32 v[192:193], v[210:211], v[218:219]
	v_pk_add_f32 v[194:195], v[208:209], v[216:217]
	v_pk_fma_f32 v[142:143], v[152:153], v[142:143], v[158:159] op_sel_hi:[0,1,0]
	v_pk_fma_f32 v[144:145], v[152:153], v[144:145], v[158:159] op_sel_hi:[0,1,0]
	v_pk_fma_f32 v[138:139], v[152:153], v[138:139], v[158:159] op_sel_hi:[0,1,0]
	v_pk_fma_f32 v[140:141], v[152:153], v[140:141], v[158:159] op_sel_hi:[0,1,0]
	v_pk_fma_f32 v[134:135], v[152:153], v[134:135], v[158:159] op_sel_hi:[0,1,0]
	v_pk_fma_f32 v[136:137], v[152:153], v[136:137], v[158:159] op_sel_hi:[0,1,0]
	v_pk_fma_f32 v[130:131], v[152:153], v[130:131], v[158:159] op_sel_hi:[0,1,0]
	v_pk_fma_f32 v[132:133], v[152:153], v[132:133], v[158:159] op_sel_hi:[0,1,0]
	v_pk_fma_f32 v[126:127], v[152:153], v[126:127], v[158:159] op_sel_hi:[0,1,0]
	v_pk_fma_f32 v[128:129], v[152:153], v[128:129], v[158:159] op_sel_hi:[0,1,0]
	v_pk_fma_f32 v[122:123], v[152:153], v[122:123], v[158:159] op_sel_hi:[0,1,0]
	v_pk_fma_f32 v[124:125], v[152:153], v[124:125], v[158:159] op_sel_hi:[0,1,0]
	v_pk_fma_f32 v[118:119], v[152:153], v[118:119], v[158:159] op_sel_hi:[0,1,0]
	v_pk_fma_f32 v[120:121], v[152:153], v[120:121], v[158:159] op_sel_hi:[0,1,0]
	v_pk_fma_f32 v[114:115], v[152:153], v[114:115], v[158:159] op_sel_hi:[0,1,0]
	v_pk_fma_f32 v[116:117], v[152:153], v[116:117], v[158:159] op_sel_hi:[0,1,0]
	v_pk_fma_f32 v[106:107], v[152:153], v[106:107], v[158:159] op_sel_hi:[0,1,0]
	v_pk_fma_f32 v[108:109], v[152:153], v[108:109], v[158:159] op_sel_hi:[0,1,0]
	v_pk_fma_f32 v[102:103], v[152:153], v[102:103], v[158:159] op_sel_hi:[0,1,0]
	v_pk_fma_f32 v[104:105], v[152:153], v[104:105], v[158:159] op_sel_hi:[0,1,0]
	v_pk_fma_f32 v[98:99], v[152:153], v[98:99], v[158:159] op_sel_hi:[0,1,0]
	v_pk_fma_f32 v[100:101], v[152:153], v[100:101], v[158:159] op_sel_hi:[0,1,0]
	v_pk_fma_f32 v[94:95], v[152:153], v[94:95], v[158:159] op_sel_hi:[0,1,0]
	v_pk_fma_f32 v[96:97], v[152:153], v[96:97], v[158:159] op_sel_hi:[0,1,0]
	v_pk_fma_f32 v[78:79], v[152:153], v[78:79], v[158:159] op_sel_hi:[0,1,0]
	v_pk_fma_f32 v[80:81], v[152:153], v[80:81], v[158:159] op_sel_hi:[0,1,0]
	v_pk_fma_f32 v[74:75], v[152:153], v[74:75], v[158:159] op_sel_hi:[0,1,0]
	v_pk_fma_f32 v[76:77], v[152:153], v[76:77], v[158:159] op_sel_hi:[0,1,0]
	v_pk_add_f32 v[14:15], v[194:195], v[14:15]
	v_pk_add_f32 v[10:11], v[184:185], v[10:11]
	v_pk_add_f32 v[16:17], v[192:193], v[16:17]
	v_pk_add_f32 v[12:13], v[172:173], v[12:13]
	v_cvt_pk_bf16_f32 v141, v140, v141
	v_cvt_pk_bf16_f32 v140, v138, v139
	v_cvt_pk_bf16_f32 v139, v144, v145
	v_cvt_pk_bf16_f32 v138, v142, v143
	v_cvt_pk_bf16_f32 v133, v132, v133
	v_cvt_pk_bf16_f32 v132, v130, v131
	v_cvt_pk_bf16_f32 v131, v136, v137
	v_cvt_pk_bf16_f32 v130, v134, v135
	v_cvt_pk_bf16_f32 v125, v124, v125
	v_cvt_pk_bf16_f32 v124, v122, v123
	v_cvt_pk_bf16_f32 v123, v128, v129
	v_cvt_pk_bf16_f32 v122, v126, v127
	v_cvt_pk_bf16_f32 v117, v116, v117
	v_cvt_pk_bf16_f32 v116, v114, v115
	v_cvt_pk_bf16_f32 v115, v120, v121
	v_cvt_pk_bf16_f32 v114, v118, v119
	v_cvt_pk_bf16_f32 v105, v104, v105
	v_cvt_pk_bf16_f32 v104, v102, v103
	v_cvt_pk_bf16_f32 v103, v108, v109
	v_cvt_pk_bf16_f32 v102, v106, v107
	v_cvt_pk_bf16_f32 v109, v96, v97
	v_cvt_pk_bf16_f32 v108, v94, v95
	v_cvt_pk_bf16_f32 v107, v100, v101
	v_cvt_pk_bf16_f32 v106, v98, v99
	v_cvt_pk_bf16_f32 v121, v76, v77
	v_cvt_pk_bf16_f32 v120, v74, v75
	v_cvt_pk_bf16_f32 v119, v80, v81
	v_cvt_pk_bf16_f32 v118, v78, v79
	v_pk_fma_f32 v[172:173], v[152:153], v[70:71], v[158:159] op_sel_hi:[0,1,0]
	v_pk_fma_f32 v[94:95], v[152:153], v[72:73], v[158:159] op_sel_hi:[0,1,0]
	v_pk_fma_f32 v[184:185], v[152:153], v[66:67], v[158:159] op_sel_hi:[0,1,0]
	v_pk_fma_f32 v[96:97], v[152:153], v[68:69], v[158:159] op_sel_hi:[0,1,0]
	ds_read_b128 v[66:69], v176
	ds_read_b128 v[70:73], v176 offset:1024
	ds_read_b128 v[74:77], v176 offset:2048
	ds_read_b128 v[78:81], v176 offset:3072
	ds_read_b128 v[98:101], v176 offset:4096
	ds_read_b128 v[126:129], v176 offset:5120
	ds_read_b128 v[134:137], v176 offset:6144
	ds_read_b128 v[142:145], v176 offset:7168
	ds_read_b128 v[166:169], v176 offset:8192
	ds_read_b128 v[192:195], v176 offset:9216
	v_cvt_pk_bf16_f32 v97, v96, v97
	v_cvt_pk_bf16_f32 v96, v184, v185
	v_cvt_pk_bf16_f32 v95, v94, v95
	v_cvt_pk_bf16_f32 v94, v172, v173
	ds_read_b128 v[196:199], v176 offset:10240
	ds_read_b128 v[200:203], v176 offset:11264
	ds_read_b128 v[204:207], v176 offset:12288
	ds_read_b128 v[208:211], v176 offset:13312
	ds_read_b128 v[212:215], v176 offset:14336
	s_waitcnt lgkmcnt(0)
	v_mfma_f32_32x32x16_bf16 v[50:65], v[66:69], v[138:141], v[50:65]
	v_mfma_f32_32x32x16_bf16 v[34:49], v[70:73], v[138:141], v[34:49]
	v_mfma_f32_32x32x16_bf16 v[18:33], v[74:77], v[138:141], v[18:33]
	v_mfma_f32_32x32x16_bf16 v[2:17], v[78:81], v[138:141], v[2:17]
	v_mfma_f32_32x32x16_bf16 v[66:81], v[98:101], v[138:141], 0
	v_mfma_f32_32x32x16_bf16 v[50:65], v[126:129], v[130:133], v[50:65]
	v_mfma_f32_32x32x16_bf16 v[34:49], v[134:137], v[130:133], v[34:49]
	v_mfma_f32_32x32x16_bf16 v[18:33], v[142:145], v[130:133], v[18:33]
	ds_read_b128 v[98:101], v176 offset:15360
	ds_read_b128 v[126:129], v176 offset:16384
	ds_read_b128 v[134:137], v176 offset:17408
	ds_read_b128 v[138:141], v176 offset:18432
	ds_read_b128 v[142:145], v176 offset:19456
	v_mfma_f32_32x32x16_bf16 v[2:17], v[166:169], v[130:133], v[2:17]
	v_mfma_f32_32x32x16_bf16 v[66:81], v[192:195], v[130:133], v[66:81]
	v_mfma_f32_32x32x16_bf16 v[50:65], v[196:199], v[122:125], v[50:65]
	v_mfma_f32_32x32x16_bf16 v[34:49], v[200:203], v[122:125], v[34:49]
	v_mfma_f32_32x32x16_bf16 v[18:33], v[204:207], v[122:125], v[18:33]
	v_mfma_f32_32x32x16_bf16 v[2:17], v[208:211], v[122:125], v[2:17]
	v_mfma_f32_32x32x16_bf16 v[66:81], v[212:215], v[122:125], v[66:81]
	s_mov_b64 s[8:9], 0x1a000
	v_readfirstlane_b32 s3, v186
	s_waitcnt lgkmcnt(0)
	v_mfma_f32_32x32x16_bf16 v[50:65], v[98:101], v[114:117], v[50:65]
	v_lshl_add_u64 v[98:99], v[180:181], 0, s[8:9]
	s_mov_b32 m0, s3
	s_waitcnt vmcnt(8) lgkmcnt(0)
	s_barrier
	global_load_lds_dwordx4 v[98:99], off
	global_load_lds_dwordx4 v[98:99], off offset:1024
	global_load_lds_dwordx4 v[98:99], off offset:2048
	global_load_lds_dwordx4 v[98:99], off offset:3072
	v_mfma_f32_32x32x16_bf16 v[34:49], v[126:129], v[114:117], v[34:49]
	ds_read_b128 v[98:101], v176 offset:20480
	ds_read_b128 v[122:125], v176 offset:21504
	v_mfma_f32_32x32x16_bf16 v[18:33], v[134:137], v[114:117], v[18:33]
	v_mfma_f32_32x32x16_bf16 v[2:17], v[138:141], v[114:117], v[2:17]
	ds_read_b128 v[126:129], v176 offset:22528
	ds_read_b128 v[130:133], v176 offset:23552
	ds_read_b128 v[134:137], v176 offset:24576
	ds_read_b128 v[138:141], v176 offset:25600
	ds_read_b128 v[166:169], v176 offset:26624
	ds_read_b128 v[192:195], v176 offset:27648
	ds_read_b128 v[196:199], v176 offset:28672
	ds_read_b128 v[200:203], v176 offset:29696
	v_mfma_f32_32x32x16_bf16 v[66:81], v[142:145], v[114:117], v[66:81]
	s_waitcnt lgkmcnt(0)
	v_mfma_f32_32x32x16_bf16 v[34:49], v[122:125], v[102:105], v[34:49]
	v_mfma_f32_32x32x16_bf16 v[18:33], v[126:129], v[102:105], v[18:33]
	v_mfma_f32_32x32x16_bf16 v[2:17], v[130:133], v[102:105], v[2:17]
	ds_read_b128 v[114:117], v176 offset:31744
	ds_read_b128 v[122:125], v176 offset:32768
	ds_read_b128 v[126:129], v176 offset:33792
	ds_read_b128 v[130:133], v176 offset:30720
	ds_read_b128 v[142:145], v176 offset:34816
	v_mfma_f32_32x32x16_bf16 v[50:65], v[98:101], v[102:105], v[50:65]
	v_mfma_f32_32x32x16_bf16 v[66:81], v[134:137], v[102:105], v[66:81]
	v_mfma_f32_32x32x16_bf16 v[50:65], v[138:141], v[106:109], v[50:65]
	v_mfma_f32_32x32x16_bf16 v[34:49], v[166:169], v[106:109], v[34:49]
	ds_read_b128 v[102:105], v176 offset:35840
	ds_read_b128 v[134:137], v176 offset:36864
	ds_read_b128 v[138:141], v176 offset:37888
	ds_read_b128 v[166:169], v176 offset:38912
	ds_read_b128 v[98:101], v176 offset:39936
	v_mfma_f32_32x32x16_bf16 v[18:33], v[192:195], v[106:109], v[18:33]
	v_mfma_f32_32x32x16_bf16 v[2:17], v[196:199], v[106:109], v[2:17]
	v_mfma_f32_32x32x16_bf16 v[66:81], v[200:203], v[106:109], v[66:81]
	s_waitcnt lgkmcnt(0)
	v_mfma_f32_32x32x16_bf16 v[50:65], v[130:133], v[118:121], v[50:65]
	v_mfma_f32_32x32x16_bf16 v[34:49], v[114:117], v[118:121], v[34:49]
	v_mfma_f32_32x32x16_bf16 v[18:33], v[122:125], v[118:121], v[18:33]
	v_mfma_f32_32x32x16_bf16 v[2:17], v[126:129], v[118:121], v[2:17]
	v_mfma_f32_32x32x16_bf16 v[66:81], v[142:145], v[118:121], v[66:81]
	s_mov_b64 s[8:9], 0x1e000
	v_readfirstlane_b32 s3, v190
	v_mfma_f32_32x32x16_bf16 v[50:65], v[102:105], v[94:97], v[50:65]
	v_lshl_add_u64 v[102:103], v[180:181], 0, s[8:9]
	s_mov_b32 m0, s3
	s_waitcnt vmcnt(4) lgkmcnt(0)
	s_barrier
	global_load_lds_dwordx4 v[102:103], off
	global_load_lds_dwordx4 v[102:103], off offset:1024
	global_load_lds_dwordx4 v[102:103], off offset:2048
	global_load_lds_dwordx4 v[102:103], off offset:3072
	s_waitcnt vmcnt(4)
	v_mfma_f32_32x32x16_bf16 v[34:49], v[134:137], v[94:97], v[34:49]
	ds_read_b128 v[102:105], v176 offset:40960
	ds_read_b128 v[106:109], v176 offset:41984
	v_mfma_f32_32x32x16_bf16 v[18:33], v[138:141], v[94:97], v[18:33]
	ds_read_b128 v[114:117], v176 offset:43008
	ds_read_b128 v[118:121], v176 offset:44032
	ds_read_b128 v[122:125], v189 offset:58112
	ds_read_b128 v[126:129], v189 offset:58128
	ds_read_b128 v[130:133], v176 offset:45056
	ds_read_b128 v[134:137], v176 offset:46080
	ds_read_b128 v[138:141], v176 offset:47104
	ds_read_b128 v[142:145], v176 offset:48128
	ds_read_b128 v[190:193], v189 offset:58176
	ds_read_b128 v[194:197], v189 offset:58192
	v_mfma_f32_32x32x16_bf16 v[2:17], v[166:169], v[94:97], v[2:17]
	v_lshlrev_b32_e32 v152, 16, v110
	v_and_b32_e32 v153, 0xffff0000, v110
	v_lshlrev_b32_e32 v158, 16, v111
	v_and_b32_e32 v159, 0xffff0000, v111
	v_lshlrev_b32_e32 v110, 16, v112
	v_and_b32_e32 v111, 0xffff0000, v112
	v_lshlrev_b32_e32 v112, 16, v113
	v_and_b32_e32 v113, 0xffff0000, v113
	s_waitcnt lgkmcnt(0)
	v_pk_mul_f32 v[166:167], v[122:123], v[152:153]
	v_pk_mul_f32 v[168:169], v[124:125], v[158:159]
	v_pk_mul_f32 v[128:129], v[128:129], v[112:113]
	v_pk_mul_f32 v[126:127], v[126:127], v[110:111]
	v_cvt_pk_bf16_f32 v113, v128, v129
	v_cvt_pk_bf16_f32 v112, v126, v127
	v_cvt_pk_bf16_f32 v111, v168, v169
	v_cvt_pk_bf16_f32 v110, v166, v167
	v_pk_fma_f32 v[152:153], v[122:123], v[152:153], v[126:127]
	v_pk_fma_f32 v[158:159], v[124:125], v[158:159], v[128:129]
	v_mfma_f32_32x32x16_bf16 v[50:65], v[102:105], v[110:113], v[50:65]
	v_mfma_f32_32x32x16_bf16 v[34:49], v[106:109], v[110:113], v[34:49]
	v_mfma_f32_32x32x16_bf16 v[18:33], v[114:117], v[110:113], v[18:33]
	ds_read_b128 v[102:105], v176 offset:49152
	ds_read_b128 v[106:109], v176 offset:50176
	ds_read_b128 v[114:117], v176 offset:51200
	ds_read_b128 v[122:125], v176 offset:52224
	ds_read_b128 v[126:129], v189 offset:58240
	ds_read_b128 v[166:169], v189 offset:58256
	v_mfma_f32_32x32x16_bf16 v[2:17], v[118:121], v[110:113], v[2:17]
	v_lshlrev_b32_e32 v110, 16, v90
	v_and_b32_e32 v111, 0xffff0000, v90
	v_lshlrev_b32_e32 v112, 16, v91
	v_and_b32_e32 v113, 0xffff0000, v91
	v_lshlrev_b32_e32 v90, 16, v92
	v_and_b32_e32 v91, 0xffff0000, v92
	v_lshlrev_b32_e32 v92, 16, v93
	v_and_b32_e32 v93, 0xffff0000, v93
	v_pk_mul_f32 v[172:173], v[196:197], v[92:93]
	v_pk_mul_f32 v[184:185], v[194:195], v[90:91]
	v_pk_mul_f32 v[118:119], v[190:191], v[110:111]
	v_pk_mul_f32 v[120:121], v[192:193], v[112:113]
	v_pk_fma_f32 v[110:111], v[190:191], v[110:111], v[184:185]
	v_pk_fma_f32 v[112:113], v[192:193], v[112:113], v[172:173]
	v_pk_add_f32 v[110:111], v[152:153], v[110:111]
	v_pk_add_f32 v[112:113], v[158:159], v[112:113]
	v_cvt_pk_bf16_f32 v90, v118, v119
	v_pk_mov_b32 v[118:119], v[110:111], v[112:113] op_sel:[1,0]
	v_mov_b32_e32 v111, v113
	v_cvt_pk_bf16_f32 v93, v172, v173
	v_cvt_pk_bf16_f32 v92, v184, v185
	v_cvt_pk_bf16_f32 v91, v120, v121
	v_pk_add_f32 v[110:111], v[118:119], v[110:111]
	s_nop 0
	v_mfma_f32_32x32x16_bf16 v[50:65], v[130:133], v[90:93], v[50:65]
	v_add_f32_e64 v152, v110, v111
	v_add_f32_e64 v153, v111, v110
	v_mfma_f32_32x32x16_bf16 v[34:49], v[134:137], v[90:93], v[34:49]
	v_mfma_f32_32x32x16_bf16 v[18:33], v[138:141], v[90:93], v[18:33]
	ds_read_b128 v[110:113], v176 offset:53248
	ds_read_b128 v[118:121], v176 offset:54272
	ds_read_b128 v[130:133], v176 offset:55296
	ds_read_b128 v[134:137], v176 offset:56320
	ds_read_b128 v[138:141], v189 offset:58304
	ds_read_b128 v[190:193], v189 offset:58320
	v_mfma_f32_32x32x16_bf16 v[2:17], v[142:145], v[90:93], v[2:17]
	v_lshlrev_b32_e32 v90, 16, v86
	v_and_b32_e32 v91, 0xffff0000, v86
	v_lshlrev_b32_e32 v92, 16, v87
	v_and_b32_e32 v93, 0xffff0000, v87
	v_lshlrev_b32_e32 v86, 16, v88
	v_and_b32_e32 v87, 0xffff0000, v88
	v_lshlrev_b32_e32 v88, 16, v89
	v_and_b32_e32 v89, 0xffff0000, v89
	s_waitcnt lgkmcnt(0)
	v_pk_mul_f32 v[142:143], v[128:129], v[92:93]
	v_pk_mul_f32 v[144:145], v[126:127], v[90:91]
	v_pk_mul_f32 v[158:159], v[166:167], v[86:87]
	v_pk_mul_f32 v[166:167], v[168:169], v[88:89]
	v_cvt_pk_bf16_f32 v88, v158, v159
	v_cvt_pk_bf16_f32 v86, v144, v145
	v_cvt_pk_bf16_f32 v89, v166, v167
	v_cvt_pk_bf16_f32 v87, v142, v143
	v_pk_fma_f32 v[92:93], v[128:129], v[92:93], v[166:167]
	v_pk_fma_f32 v[90:91], v[126:127], v[90:91], v[158:159]
	v_mfma_f32_32x32x16_bf16 v[50:65], v[102:105], v[86:89], v[50:65]
	v_mfma_f32_32x32x16_bf16 v[34:49], v[106:109], v[86:89], v[34:49]
	v_mfma_f32_32x32x16_bf16 v[18:33], v[114:117], v[86:89], v[18:33]
	v_mfma_f32_32x32x16_bf16 v[2:17], v[122:125], v[86:89], v[2:17]
	v_lshlrev_b32_e32 v86, 16, v82
	v_and_b32_e32 v87, 0xffff0000, v82
	v_lshlrev_b32_e32 v88, 16, v83
	v_and_b32_e32 v89, 0xffff0000, v83
	v_lshlrev_b32_e32 v82, 16, v84
	v_and_b32_e32 v83, 0xffff0000, v84
	v_lshlrev_b32_e32 v84, 16, v85
	v_and_b32_e32 v85, 0xffff0000, v85
	v_mfma_f32_32x32x16_bf16 v[66:81], v[98:101], v[94:97], v[66:81]
	v_mul_f32_e64 v102, v140, v88
	v_mul_f32_e64 v103, v141, v89
	v_mul_f32_e64 v104, v138, v86
	v_mul_f32_e64 v105, v139, v87
	v_mul_f32_e64 v106, v190, v82
	v_mul_f32_e64 v107, v191, v83
	v_pk_mul_f32 v[108:109], v[192:193], v[84:85]
	v_cvt_pk_bf16_f32 v84, v106, v107
	v_cvt_pk_bf16_f32 v82, v104, v105
	v_cvt_pk_bf16_f32 v85, v108, v109
	v_cvt_pk_bf16_f32 v83, v102, v103
	s_waitcnt vmcnt(4) lgkmcnt(0)
	s_nop 0
	v_mfma_f32_32x32x16_bf16 v[50:65], v[110:113], v[82:85], v[50:65]
	s_barrier
	v_permlane32_swap_b32_e32 v162, v150
	v_permlane32_swap_b32_e32 v170, v148
	v_mov_b32_e32 v171, v162
	v_mov_b32_e32 v149, v150
	v_mfma_f32_32x32x16_bf16 v[34:49], v[118:121], v[82:85], v[34:49]
	v_add_f32_e64 v70, v170, v148
	v_add_f32_e64 v71, v171, v149
	s_mov_b32 s8, 0x3e3504f3
	v_add_f32_e64 v66, v66, v70
	v_add_f32_e64 v67, v67, v71
	v_or_b32_e32 v182, v182, v188
	v_mul_f32_e32 v74, v51, v51
	v_fmac_f32_e32 v74, v50, v50
	v_fmac_f32_e32 v74, v52, v52
	v_mfma_f32_32x32x16_bf16 v[18:33], v[130:133], v[82:85], v[18:33]
	v_fmac_f32_e32 v74, v53, v53
	v_fmac_f32_e32 v74, v54, v54
	v_fmac_f32_e32 v74, v55, v55
	v_fmac_f32_e32 v74, v56, v56
	v_fmac_f32_e32 v74, v57, v57
	v_fmac_f32_e32 v74, v58, v58
	v_fmac_f32_e32 v74, v59, v59
	v_mfma_f32_32x32x16_bf16 v[2:17], v[134:137], v[82:85], v[2:17]
	ds_read_b128 v[82:85], v147 offset:59904
	v_fmac_f32_e32 v74, v60, v60
	v_fmac_f32_e32 v74, v61, v61
	v_fmac_f32_e32 v74, v62, v62
	v_fmac_f32_e32 v74, v63, v63
	s_waitcnt lgkmcnt(0)
	v_pk_add_f32 v[66:67], v[82:83], v[66:67]
	v_fmac_f32_e32 v74, v64, v64
	v_pk_mul_f32 v[130:131], v[66:67], s[8:9] op_sel_hi:[1,0]
	v_lshlrev_b64 v[66:67], 5, v[182:183]
	v_lshl_add_u64 v[134:135], s[4:5], 0, v[66:67]
	v_add_f32_e32 v66, 0, v50
	v_add_f32_e32 v66, v66, v51
	v_add_f32_e32 v66, v66, v52
	v_add_f32_e32 v66, v66, v53
	v_add_f32_e32 v66, v66, v54
	v_add_f32_e32 v66, v66, v55
	v_add_f32_e32 v66, v66, v56
	v_add_f32_e32 v66, v66, v57
	v_add_f32_e32 v66, v66, v58
	v_add_f32_e32 v66, v66, v59
	v_add_f32_e32 v66, v66, v60
	v_add_f32_e32 v66, v66, v61
	v_add_f32_e32 v66, v66, v62
	v_add_f32_e32 v66, v66, v63
	v_add_f32_e32 v66, v66, v64
	v_add_f32_e32 v66, v66, v65
	v_fmac_f32_e32 v74, v65, v65
	v_add_f32_e32 v66, v66, v34
	v_fmac_f32_e32 v74, v34, v34
	v_add_f32_e32 v66, v66, v35
	v_fmac_f32_e32 v74, v35, v35
	v_add_f32_e32 v66, v66, v36
	v_fmac_f32_e32 v74, v36, v36
	v_add_f32_e32 v66, v66, v37
	v_fmac_f32_e32 v74, v37, v37
	v_add_f32_e32 v66, v66, v38
	v_fmac_f32_e32 v74, v38, v38
	v_add_f32_e32 v66, v66, v39
	v_fmac_f32_e32 v74, v39, v39
	v_add_f32_e32 v66, v66, v40
	v_fmac_f32_e32 v74, v40, v40
	v_add_f32_e32 v66, v66, v41
	v_fmac_f32_e32 v74, v41, v41
	v_add_f32_e32 v66, v66, v42
	v_fmac_f32_e32 v74, v42, v42
	v_add_f32_e32 v66, v66, v43
	v_fmac_f32_e32 v74, v43, v43
	v_add_f32_e32 v66, v66, v44
	v_fmac_f32_e32 v74, v44, v44
	v_add_f32_e32 v66, v66, v45
	v_fmac_f32_e32 v74, v45, v45
	v_add_f32_e32 v66, v66, v46
	v_fmac_f32_e32 v74, v46, v46
	v_add_f32_e32 v66, v66, v47
	v_fmac_f32_e32 v74, v47, v47
	v_add_f32_e32 v66, v66, v48
	v_fmac_f32_e32 v74, v48, v48
	v_add_f32_e32 v66, v66, v49
	v_fmac_f32_e32 v74, v49, v49
	v_add_f32_e32 v66, v66, v18
	v_fmac_f32_e32 v74, v18, v18
	v_add_f32_e32 v66, v66, v19
	v_fmac_f32_e32 v74, v19, v19
	v_add_f32_e32 v66, v66, v20
	v_fmac_f32_e32 v74, v20, v20
	v_add_f32_e32 v66, v66, v21
	v_fmac_f32_e32 v74, v21, v21
	v_add_f32_e32 v66, v66, v22
	v_fmac_f32_e32 v74, v22, v22
	v_add_f32_e32 v66, v66, v23
	v_fmac_f32_e32 v74, v23, v23
	v_add_f32_e32 v66, v66, v24
	v_fmac_f32_e32 v74, v24, v24
	v_add_f32_e32 v66, v66, v25
	v_fmac_f32_e32 v74, v25, v25
	v_add_f32_e32 v66, v66, v26
	v_fmac_f32_e32 v74, v26, v26
	v_add_f32_e32 v66, v66, v27
	v_fmac_f32_e32 v74, v27, v27
	v_add_f32_e32 v66, v66, v28
	v_fmac_f32_e32 v74, v28, v28
	v_add_f32_e32 v66, v66, v29
	v_fmac_f32_e32 v74, v29, v29
	v_add_f32_e32 v66, v66, v30
	v_fmac_f32_e32 v74, v30, v30
	v_add_f32_e32 v66, v66, v31
	v_fmac_f32_e32 v74, v31, v31
	v_add_f32_e32 v66, v66, v32
	v_fmac_f32_e32 v74, v32, v32
	v_add_f32_e32 v66, v66, v33
	v_fmac_f32_e32 v74, v33, v33
	v_add_f32_e32 v66, v66, v2
	v_fmac_f32_e32 v74, v2, v2
	v_pk_fma_f32 v[88:89], v[140:141], v[88:89], v[108:109]
	v_pk_fma_f32 v[86:87], v[138:139], v[86:87], v[106:107]
	v_add_f32_e32 v66, v66, v3
	v_fmac_f32_e32 v74, v3, v3
	v_pk_add_f32 v[86:87], v[90:91], v[86:87]
	v_pk_add_f32 v[88:89], v[92:93], v[88:89]
	v_add_f32_e32 v66, v66, v4
	v_fmac_f32_e32 v74, v4, v4
	v_pk_mov_b32 v[90:91], v[86:87], v[88:89] op_sel:[1,0]
	v_mov_b32_e32 v87, v89
	v_add_f32_e32 v66, v66, v5
	v_fmac_f32_e32 v74, v5, v5
	v_pk_add_f32 v[86:87], v[90:91], v[86:87]
	v_add_f32_e32 v66, v66, v6
	v_fmac_f32_e32 v74, v6, v6
	v_pk_add_f32 v[86:87], v[86:87], v[86:87] op_sel:[0,1] op_sel_hi:[1,0]
	v_add_f32_e32 v66, v66, v7
	v_fmac_f32_e32 v74, v7, v7
	v_permlane32_swap_b32_e32 v146, v86
	v_add_f32_e32 v66, v66, v8
	v_fmac_f32_e32 v74, v8, v8
	v_permlane32_swap_b32_e32 v156, v152
	v_mov_b32_e32 v157, v146
	v_mov_b32_e32 v153, v86
	v_add_f32_e32 v66, v66, v9
	v_fmac_f32_e32 v74, v9, v9
	v_pk_mul_f32 v[72:73], v[10:11], v[10:11]
	v_pk_add_f32 v[70:71], v[156:157], v[152:153]
	v_add_f32_e32 v66, v66, v10
	v_add_f32_e32 v72, v74, v72
	v_pk_add_f32 v[68:69], v[68:69], v[70:71]
	v_add_f32_e32 v75, v66, v11
	v_pk_mul_f32 v[70:71], v[12:13], v[12:13]
	v_add_f32_e32 v72, v72, v73
	v_pk_add_f32 v[68:69], v[84:85], v[68:69]
	v_add_f32_e32 v73, v75, v12
	v_add_f32_e32 v70, v72, v70
	v_pk_mul_f32 v[132:133], v[68:69], s[8:9] op_sel_hi:[1,0]
	v_pk_mul_f32 v[68:69], v[14:15], v[14:15]
	v_add_f32_e32 v73, v73, v13
	v_add_f32_e32 v70, v70, v71
	v_add_f32_e32 v71, v73, v14
	v_add_f32_e32 v68, v70, v68
	v_pk_mul_f32 v[66:67], v[16:17], v[16:17]
	v_add_f32_e32 v71, v71, v15
	v_add_f32_e32 v68, v68, v69
	v_add_f32_e32 v69, v71, v16
	v_add_f32_e32 v66, v68, v66
	v_add_f32_e32 v69, v69, v17
	v_add_f32_e32 v68, v66, v67
	v_mov_b32_e32 v67, v69
	v_mov_b32_e32 v66, v68
	s_nop 0
	v_permlane32_swap_b32_e32 v69, v67
	v_permlane32_swap_b32_e32 v68, v66
	v_pk_add_f32 v[66:67], v[68:69], v[66:67]
	v_mov_b32_e32 v155, v175
	v_pk_mul_f32 v[136:137], v[66:67], s[0:1] op_sel_hi:[1,0]
	v_readfirstlane_b32 s0, v187
	v_fma_f32 v66, -v137, v137, v136
	v_add_f32_e32 v66, 0x3727c5ac, v66
	v_cmp_gt_f32_e32 vcc, s2, v66
	s_mov_b64 s[2:3], 0x22000
	v_mul_f32_e32 v67, 0x4b800000, v66
	v_lshl_add_u64 v[138:139], v[180:181], 0, s[2:3]
	s_mov_b32 m0, s0
	v_cndmask_b32_e32 v136, v66, v67, vcc
	ds_read_b128 v[114:117], v147 offset:58880
	ds_read_b128 v[118:121], v147 offset:58912
	ds_read_b128 v[122:125], v147 offset:58944
	ds_read_b128 v[126:129], v147 offset:58976
	ds_read_b128 v[98:101], v147 offset:59008
	ds_read_b128 v[102:105], v147 offset:59040
	ds_read_b128 v[106:109], v147 offset:59072
	ds_read_b128 v[110:113], v147 offset:59104
	ds_read_b128 v[82:85], v147 offset:59136
	ds_read_b128 v[86:89], v147 offset:59168
	ds_read_b128 v[90:93], v147 offset:59200
	ds_read_b128 v[94:97], v147 offset:59232
	ds_read_b128 v[66:69], v147 offset:59264
	ds_read_b128 v[70:73], v147 offset:59296
	ds_read_b128 v[74:77], v147 offset:59328
	ds_read_b128 v[78:81], v147 offset:59360
	global_load_lds_dwordx4 v[138:139], off
	global_load_lds_dwordx4 v[138:139], off offset:1024
	global_load_lds_dwordx4 v[138:139], off offset:2048
	global_load_lds_dwordx4 v[138:139], off offset:3072
	v_rsq_f32_e32 v136, v136
	v_lshl_add_u64 v[134:135], v[134:135], 0, v[154:155]
	global_store_dwordx4 v[134:135], v[130:133], off sc1
	s_nop 1
	v_mul_f32_e32 v130, 0x45800000, v136
	v_cndmask_b32_e32 v162, v136, v130, vcc
	v_mul_f32_e64 v166, v162, -v137
	v_pk_fma_f32 v[134:135], v[162:163], v[50:51], v[166:167] op_sel_hi:[0,1,0]
	v_pk_fma_f32 v[130:131], v[162:163], v[52:53], v[166:167] op_sel_hi:[0,1,0]
	v_pk_fma_f32 v[136:137], v[162:163], v[54:55], v[166:167] op_sel_hi:[0,1,0]
	v_pk_fma_f32 v[132:133], v[162:163], v[56:57], v[166:167] op_sel_hi:[0,1,0]
	v_cvt_pk_bf16_f32 v133, v132, v133
	v_cvt_pk_bf16_f32 v132, v136, v137
	v_cvt_pk_bf16_f32 v131, v130, v131
	v_cvt_pk_bf16_f32 v130, v134, v135
	v_pk_fma_f32 v[138:139], v[162:163], v[58:59], v[166:167] op_sel_hi:[0,1,0]
	v_pk_fma_f32 v[134:135], v[162:163], v[60:61], v[166:167] op_sel_hi:[0,1,0]
	v_pk_fma_f32 v[140:141], v[162:163], v[62:63], v[166:167] op_sel_hi:[0,1,0]
	v_pk_fma_f32 v[136:137], v[162:163], v[64:65], v[166:167] op_sel_hi:[0,1,0]
	v_cvt_pk_bf16_f32 v137, v136, v137
	v_cvt_pk_bf16_f32 v136, v140, v141
	v_cvt_pk_bf16_f32 v135, v134, v135
	v_cvt_pk_bf16_f32 v134, v138, v139
	v_pk_fma_f32 v[142:143], v[162:163], v[34:35], v[166:167] op_sel_hi:[0,1,0]
	v_pk_fma_f32 v[138:139], v[162:163], v[36:37], v[166:167] op_sel_hi:[0,1,0]
	v_pk_fma_f32 v[144:145], v[162:163], v[38:39], v[166:167] op_sel_hi:[0,1,0]
	v_pk_fma_f32 v[140:141], v[162:163], v[40:41], v[166:167] op_sel_hi:[0,1,0]
	v_cvt_pk_bf16_f32 v141, v140, v141
	v_cvt_pk_bf16_f32 v140, v144, v145
	v_cvt_pk_bf16_f32 v139, v138, v139
	v_cvt_pk_bf16_f32 v138, v142, v143
	v_pk_fma_f32 v[146:147], v[162:163], v[42:43], v[166:167] op_sel_hi:[0,1,0]
	v_pk_fma_f32 v[142:143], v[162:163], v[44:45], v[166:167] op_sel_hi:[0,1,0]
	v_pk_fma_f32 v[148:149], v[162:163], v[46:47], v[166:167] op_sel_hi:[0,1,0]
	v_pk_fma_f32 v[144:145], v[162:163], v[48:49], v[166:167] op_sel_hi:[0,1,0]
	v_cvt_pk_bf16_f32 v145, v144, v145
	v_cvt_pk_bf16_f32 v144, v148, v149
	v_cvt_pk_bf16_f32 v143, v142, v143
	v_cvt_pk_bf16_f32 v142, v146, v147
	v_pk_fma_f32 v[150:151], v[162:163], v[18:19], v[166:167] op_sel_hi:[0,1,0]
	v_pk_fma_f32 v[146:147], v[162:163], v[20:21], v[166:167] op_sel_hi:[0,1,0]
	v_pk_fma_f32 v[152:153], v[162:163], v[22:23], v[166:167] op_sel_hi:[0,1,0]
	v_pk_fma_f32 v[148:149], v[162:163], v[24:25], v[166:167] op_sel_hi:[0,1,0]
	v_cvt_pk_bf16_f32 v149, v148, v149
	v_cvt_pk_bf16_f32 v148, v152, v153
	v_cvt_pk_bf16_f32 v147, v146, v147
	v_cvt_pk_bf16_f32 v146, v150, v151
	v_pk_fma_f32 v[156:157], v[162:163], v[26:27], v[166:167] op_sel_hi:[0,1,0]
	v_pk_fma_f32 v[150:151], v[162:163], v[28:29], v[166:167] op_sel_hi:[0,1,0]
	v_pk_fma_f32 v[158:159], v[162:163], v[30:31], v[166:167] op_sel_hi:[0,1,0]
	v_pk_fma_f32 v[152:153], v[162:163], v[32:33], v[166:167] op_sel_hi:[0,1,0]
	v_cvt_pk_bf16_f32 v153, v152, v153
	v_cvt_pk_bf16_f32 v152, v158, v159
	v_cvt_pk_bf16_f32 v151, v150, v151
	v_cvt_pk_bf16_f32 v150, v156, v157
	v_pk_fma_f32 v[168:169], v[162:163], v[2:3], v[166:167] op_sel_hi:[0,1,0]
	v_pk_fma_f32 v[156:157], v[162:163], v[4:5], v[166:167] op_sel_hi:[0,1,0]
	v_pk_fma_f32 v[170:171], v[162:163], v[6:7], v[166:167] op_sel_hi:[0,1,0]
	v_pk_fma_f32 v[158:159], v[162:163], v[8:9], v[166:167] op_sel_hi:[0,1,0]
	v_cvt_pk_bf16_f32 v159, v158, v159
	v_cvt_pk_bf16_f32 v158, v170, v171
	v_cvt_pk_bf16_f32 v157, v156, v157
	v_cvt_pk_bf16_f32 v156, v168, v169
	v_pk_fma_f32 v[212:213], v[162:163], v[10:11], v[166:167] op_sel_hi:[0,1,0]
	v_pk_fma_f32 v[208:209], v[162:163], v[12:13], v[166:167] op_sel_hi:[0,1,0]
	v_pk_fma_f32 v[214:215], v[162:163], v[14:15], v[166:167] op_sel_hi:[0,1,0]
	v_pk_fma_f32 v[210:211], v[162:163], v[16:17], v[166:167] op_sel_hi:[0,1,0]
	ds_read_b128 v[166:169], v176
	ds_read_b128 v[170:173], v176 offset:1024
	ds_read_b128 v[182:185], v176 offset:2048
	ds_read_b128 v[188:191], v176 offset:3072
	ds_read_b128 v[192:195], v176 offset:4096
	ds_read_b128 v[196:199], v176 offset:5120
	ds_read_b128 v[200:203], v176 offset:6144
	ds_read_b128 v[204:207], v176 offset:7168
	v_cvt_pk_bf16_f32 v211, v210, v211
	v_cvt_pk_bf16_f32 v210, v214, v215
	v_cvt_pk_bf16_f32 v209, v208, v209
	v_cvt_pk_bf16_f32 v208, v212, v213
	s_waitcnt lgkmcnt(0)
	v_mfma_f32_32x32x16_bf16 v[114:129], v[166:169], v[130:133], v[114:129]
	v_mfma_f32_32x32x16_bf16 v[98:113], v[170:173], v[130:133], v[98:113]
	v_mfma_f32_32x32x16_bf16 v[82:97], v[182:185], v[130:133], v[82:97]
	ds_read_b128 v[166:169], v176 offset:8192
	ds_read_b128 v[170:173], v176 offset:9216
	ds_read_b128 v[182:185], v176 offset:10240
	ds_read_b128 v[212:215], v176 offset:11264
	v_mfma_f32_32x32x16_bf16 v[66:81], v[188:191], v[130:133], v[66:81]
	v_mfma_f32_32x32x16_bf16 v[114:129], v[192:195], v[134:137], v[114:129]
	v_mfma_f32_32x32x16_bf16 v[98:113], v[196:199], v[134:137], v[98:113]
	ds_read_b128 v[130:133], v176 offset:12288
	ds_read_b128 v[188:191], v176 offset:13312
	ds_read_b128 v[192:195], v176 offset:14336
	ds_read_b128 v[196:199], v176 offset:15360
	v_mfma_f32_32x32x16_bf16 v[82:97], v[200:203], v[134:137], v[82:97]
	v_mfma_f32_32x32x16_bf16 v[66:81], v[204:207], v[134:137], v[66:81]
	s_waitcnt lgkmcnt(0)
	v_mfma_f32_32x32x16_bf16 v[114:129], v[166:169], v[138:141], v[114:129]
	v_mfma_f32_32x32x16_bf16 v[98:113], v[170:173], v[138:141], v[98:113]
	v_mfma_f32_32x32x16_bf16 v[82:97], v[182:185], v[138:141], v[82:97]
	v_mfma_f32_32x32x16_bf16 v[66:81], v[212:215], v[138:141], v[66:81]
	s_mov_b64 s[2:3], 0x26000
	v_readfirstlane_b32 s0, v186
	v_mfma_f32_32x32x16_bf16 v[114:129], v[130:133], v[142:145], v[114:129]
	v_lshl_add_u64 v[130:131], v[180:181], 0, s[2:3]
	s_mov_b32 m0, s0
	s_waitcnt vmcnt(4) lgkmcnt(0)
	s_barrier
	global_load_lds_dwordx4 v[130:131], off
	global_load_lds_dwordx4 v[130:131], off offset:1024
	global_load_lds_dwordx4 v[130:131], off offset:2048
	global_load_lds_dwordx4 v[130:131], off offset:3072
	v_mfma_f32_32x32x16_bf16 v[98:113], v[188:191], v[142:145], v[98:113]
	ds_read_b128 v[130:133], v176 offset:20480
	ds_read_b128 v[134:137], v176 offset:21504
	ds_read_b128 v[138:141], v176 offset:22528
	ds_read_b128 v[166:169], v176 offset:23552
	ds_read_b128 v[170:173], v176 offset:24576
	ds_read_b128 v[180:183], v176 offset:25600
	ds_read_b128 v[184:187], v176 offset:26624
	ds_read_b128 v[188:191], v176 offset:27648
	v_mfma_f32_32x32x16_bf16 v[82:97], v[192:195], v[142:145], v[82:97]
	v_mfma_f32_32x32x16_bf16 v[66:81], v[196:199], v[142:145], v[66:81]
	s_waitcnt lgkmcnt(0)
	v_mfma_f32_32x32x16_bf16 v[114:129], v[130:133], v[146:149], v[114:129]
	v_mfma_f32_32x32x16_bf16 v[98:113], v[134:137], v[146:149], v[98:113]
	v_mfma_f32_32x32x16_bf16 v[82:97], v[138:141], v[146:149], v[82:97]
	ds_read_b128 v[130:133], v176 offset:28672
	ds_read_b128 v[134:137], v176 offset:29696
	ds_read_b128 v[138:141], v176 offset:30720
	ds_read_b128 v[142:145], v176 offset:31744
	v_mfma_f32_32x32x16_bf16 v[66:81], v[166:169], v[146:149], v[66:81]
	v_mfma_f32_32x32x16_bf16 v[114:129], v[170:173], v[150:153], v[114:129]
	v_mfma_f32_32x32x16_bf16 v[98:113], v[180:183], v[150:153], v[98:113]
	ds_read_b128 v[146:149], v176 offset:32768
	ds_read_b128 v[166:169], v176 offset:33792
	ds_read_b128 v[170:173], v176 offset:34816
	ds_read_b128 v[180:183], v176 offset:35840
	v_mfma_f32_32x32x16_bf16 v[82:97], v[184:187], v[150:153], v[82:97]
	v_mfma_f32_32x32x16_bf16 v[66:81], v[188:191], v[150:153], v[66:81]
	s_waitcnt lgkmcnt(0)
	v_mfma_f32_32x32x16_bf16 v[114:129], v[130:133], v[156:159], v[114:129]
	v_mfma_f32_32x32x16_bf16 v[98:113], v[134:137], v[156:159], v[98:113]
	v_mfma_f32_32x32x16_bf16 v[82:97], v[138:141], v[156:159], v[82:97]
	v_mfma_f32_32x32x16_bf16 v[66:81], v[142:145], v[156:159], v[66:81]
	v_mfma_f32_32x32x16_bf16 v[114:129], v[146:149], v[208:211], v[114:129]
	s_waitcnt vmcnt(4) lgkmcnt(0)
	s_barrier
	v_mfma_f32_32x32x16_bf16 v[98:113], v[166:169], v[208:211], v[98:113]
	s_nop 8
	v_mul_f32_e32 v130, 0x3c23d70a, v114
	v_mul_f32_e32 v131, 0x3c23d70a, v115
	v_max_f32_e32 v114, v114, v130
	v_mul_f32_e32 v130, 0x3c23d70a, v116
	v_max_f32_e32 v115, v115, v131
	v_max_f32_e32 v116, v116, v130
	v_mul_f32_e32 v130, 0x3c23d70a, v117
	v_max_f32_e32 v117, v117, v130
	v_cvt_pk_bf16_f32 v134, v114, v115
	v_mul_f32_e32 v114, 0x3c23d70a, v122
	v_cvt_pk_bf16_f32 v135, v116, v117
	v_max_f32_e32 v114, v122, v114
	v_mul_f32_e32 v115, 0x3c23d70a, v123
	v_mfma_f32_32x32x16_bf16 v[82:97], v[170:173], v[208:211], v[82:97]
	v_max_f32_e32 v115, v123, v115
	v_cvt_pk_bf16_f32 v138, v114, v115
	v_mul_f32_e32 v114, 0x3c23d70a, v98
	v_max_f32_e32 v98, v98, v114
	v_mul_f32_e32 v114, 0x3c23d70a, v99
	v_max_f32_e32 v99, v99, v114
	v_mul_f32_e32 v114, 0x3c23d70a, v100
	v_max_f32_e32 v100, v100, v114
	v_mul_f32_e32 v114, 0x3c23d70a, v101
	v_max_f32_e32 v101, v101, v114
	v_cvt_pk_bf16_f32 v142, v98, v99
	v_mul_f32_e32 v98, 0x3c23d70a, v106
	v_cvt_pk_bf16_f32 v143, v100, v101
	v_max_f32_e32 v98, v106, v98
	v_mul_f32_e32 v99, 0x3c23d70a, v107
	v_mfma_f32_32x32x16_bf16 v[66:81], v[180:183], v[208:211], v[66:81]
	v_max_f32_e32 v99, v107, v99
	v_cvt_pk_bf16_f32 v146, v98, v99
	v_mul_f32_e32 v98, 0x3c23d70a, v82
	v_max_f32_e32 v82, v82, v98
	v_mul_f32_e32 v98, 0x3c23d70a, v83
	v_max_f32_e32 v83, v83, v98
	v_mul_f32_e32 v98, 0x3c23d70a, v84
	v_max_f32_e32 v84, v84, v98
	v_mul_f32_e32 v98, 0x3c23d70a, v85
	v_max_f32_e32 v85, v85, v98
	v_cvt_pk_bf16_f32 v150, v82, v83
	v_mul_f32_e32 v82, 0x3c23d70a, v90
	v_cvt_pk_bf16_f32 v151, v84, v85
	v_max_f32_e32 v82, v90, v82
	v_mul_f32_e32 v83, 0x3c23d70a, v91
	v_max_f32_e32 v83, v91, v83
	v_mul_f32_e32 v130, 0x3c23d70a, v118
	v_cvt_pk_bf16_f32 v156, v82, v83
	v_mul_f32_e32 v82, 0x3c23d70a, v66
	v_max_f32_e32 v118, v118, v130
	v_mul_f32_e32 v130, 0x3c23d70a, v119
	v_max_f32_e32 v66, v66, v82
	v_mul_f32_e32 v82, 0x3c23d70a, v67
	v_max_f32_e32 v119, v119, v130
	v_mul_f32_e32 v130, 0x3c23d70a, v120
	v_mul_f32_e32 v114, 0x3c23d70a, v102
	v_mul_f32_e32 v98, 0x3c23d70a, v86
	v_max_f32_e32 v67, v67, v82
	v_max_f32_e32 v120, v120, v130
	v_mul_f32_e32 v130, 0x3c23d70a, v121
	v_max_f32_e32 v102, v102, v114
	v_mul_f32_e32 v114, 0x3c23d70a, v103
	v_max_f32_e32 v86, v86, v98
	v_mul_f32_e32 v98, 0x3c23d70a, v87
	v_cvt_pk_bf16_f32 v166, v66, v67
	v_mul_f32_e32 v66, 0x3c23d70a, v74
	v_max_f32_e32 v121, v121, v130
	v_mul_f32_e32 v116, 0x3c23d70a, v124
	v_max_f32_e32 v103, v103, v114
	v_mul_f32_e32 v114, 0x3c23d70a, v104
	v_mul_f32_e32 v100, 0x3c23d70a, v108
	v_max_f32_e32 v87, v87, v98
	v_mul_f32_e32 v98, 0x3c23d70a, v88
	v_mul_f32_e32 v84, 0x3c23d70a, v92
	v_mul_f32_e32 v82, 0x3c23d70a, v68
	v_max_f32_e32 v130, v74, v66
	v_mul_f32_e32 v66, 0x3c23d70a, v75
	v_cvt_pk_bf16_f32 v136, v118, v119
	v_max_f32_e32 v116, v124, v116
	v_mul_f32_e32 v117, 0x3c23d70a, v125
	v_max_f32_e32 v104, v104, v114
	v_mul_f32_e32 v114, 0x3c23d70a, v105
	v_cvt_pk_bf16_f32 v144, v102, v103
	v_max_f32_e32 v100, v108, v100
	v_mul_f32_e32 v101, 0x3c23d70a, v109
	v_max_f32_e32 v88, v88, v98
	v_mul_f32_e32 v98, 0x3c23d70a, v89
	v_cvt_pk_bf16_f32 v152, v86, v87
	v_max_f32_e32 v84, v92, v84
	v_mul_f32_e32 v85, 0x3c23d70a, v93
	v_max_f32_e32 v68, v68, v82
	v_mul_f32_e32 v82, 0x3c23d70a, v69
	v_max_f32_e32 v155, v75, v66
	v_mul_f32_e32 v66, 0x3c23d70a, v76
	v_max_f32_e32 v117, v125, v117
	v_mul_f32_e32 v118, 0x3c23d70a, v126
	v_max_f32_e32 v105, v105, v114
	v_max_f32_e32 v101, v109, v101
	v_mul_f32_e32 v102, 0x3c23d70a, v110
	v_max_f32_e32 v89, v89, v98
	v_max_f32_e32 v85, v93, v85
	v_mul_f32_e32 v86, 0x3c23d70a, v94
	v_max_f32_e32 v69, v69, v82
	v_mul_f32_e32 v82, 0x3c23d70a, v70
	v_max_f32_e32 v131, v76, v66
	v_mul_f32_e32 v66, 0x3c23d70a, v77
	v_cvt_pk_bf16_f32 v137, v120, v121
	v_max_f32_e32 v118, v126, v118
	v_mul_f32_e32 v119, 0x3c23d70a, v127
	v_cvt_pk_bf16_f32 v145, v104, v105
	v_max_f32_e32 v102, v110, v102
	v_mul_f32_e32 v103, 0x3c23d70a, v111
	v_cvt_pk_bf16_f32 v153, v88, v89
	v_max_f32_e32 v86, v94, v86
	v_mul_f32_e32 v87, 0x3c23d70a, v95
	v_max_f32_e32 v70, v70, v82
	v_mul_f32_e32 v82, 0x3c23d70a, v71
	v_max_f32_e32 v162, v77, v66
	v_mul_f32_e32 v66, 0x3c23d70a, v78
	v_max_f32_e32 v119, v127, v119
	v_mul_f32_e32 v120, 0x3c23d70a, v128
	v_max_f32_e32 v103, v111, v103
	v_mul_f32_e32 v104, 0x3c23d70a, v112
	v_max_f32_e32 v87, v95, v87
	v_mul_f32_e32 v88, 0x3c23d70a, v96
	v_max_f32_e32 v71, v71, v82
	v_mul_f32_e32 v82, 0x3c23d70a, v72
	v_max_f32_e32 v132, v78, v66
	v_mul_f32_e32 v66, 0x3c23d70a, v79
	v_max_f32_e32 v120, v128, v120
	v_mul_f32_e32 v121, 0x3c23d70a, v129
	v_max_f32_e32 v104, v112, v104
	v_mul_f32_e32 v105, 0x3c23d70a, v113
	v_max_f32_e32 v88, v96, v88
	v_mul_f32_e32 v89, 0x3c23d70a, v97
	v_max_f32_e32 v72, v72, v82
	v_mul_f32_e32 v82, 0x3c23d70a, v73
	v_max_f32_e32 v174, v79, v66
	v_mul_f32_e32 v66, 0x3c23d70a, v80
	v_max_f32_e32 v121, v129, v121
	v_max_f32_e32 v105, v113, v105
	v_max_f32_e32 v89, v97, v89
	v_max_f32_e32 v73, v73, v82
	v_max_f32_e32 v133, v80, v66
	v_mul_f32_e32 v66, 0x3c23d70a, v81
	v_cvt_pk_bf16_f32 v141, v120, v121
	v_cvt_pk_bf16_f32 v140, v118, v119
	v_cvt_pk_bf16_f32 v139, v116, v117
	v_cvt_pk_bf16_f32 v149, v104, v105
	v_cvt_pk_bf16_f32 v148, v102, v103
	v_cvt_pk_bf16_f32 v147, v100, v101
	v_cvt_pk_bf16_f32 v159, v88, v89
	v_cvt_pk_bf16_f32 v158, v86, v87
	v_cvt_pk_bf16_f32 v157, v84, v85
	v_cvt_pk_bf16_f32 v169, v72, v73
	v_cvt_pk_bf16_f32 v168, v70, v71
	v_cvt_pk_bf16_f32 v167, v68, v69
	v_max_f32_e32 v177, v81, v66
	ds_read_b128 v[114:117], v154 offset:59392
	ds_read_b128 v[118:121], v154 offset:59424
	ds_read_b128 v[122:125], v154 offset:59456
	ds_read_b128 v[126:129], v154 offset:59488
	ds_read_b128 v[98:101], v154 offset:59520
	ds_read_b128 v[102:105], v154 offset:59552
	ds_read_b128 v[106:109], v154 offset:59584
	ds_read_b128 v[110:113], v154 offset:59616
	ds_read_b128 v[82:85], v154 offset:59648
	ds_read_b128 v[86:89], v154 offset:59680
	ds_read_b128 v[90:93], v154 offset:59712
	ds_read_b128 v[94:97], v154 offset:59744
	ds_read_b128 v[66:69], v154 offset:59776
	ds_read_b128 v[70:73], v154 offset:59808
	ds_read_b128 v[74:77], v154 offset:59840
	ds_read_b128 v[78:81], v154 offset:59872
	ds_read_b128 v[170:173], v176 offset:40960
	ds_read_b128 v[180:183], v176 offset:41984
	ds_read_b128 v[184:187], v176 offset:43008
	ds_read_b128 v[188:191], v176 offset:44032
	ds_read_b128 v[192:195], v176 offset:45056
	ds_read_b128 v[196:199], v176 offset:46080
	ds_read_b128 v[200:203], v176 offset:47104
	ds_read_b128 v[204:207], v176 offset:48128
	v_cvt_pk_bf16_f32 v133, v133, v177
	v_cvt_pk_bf16_f32 v132, v132, v174
	v_cvt_pk_bf16_f32 v131, v131, v162
	v_cvt_pk_bf16_f32 v130, v130, v155
	s_waitcnt lgkmcnt(0)
	v_mfma_f32_32x32x16_bf16 v[114:129], v[170:173], v[134:137], v[114:129]
	v_mfma_f32_32x32x16_bf16 v[98:113], v[180:183], v[134:137], v[98:113]
	v_mfma_f32_32x32x16_bf16 v[82:97], v[184:187], v[134:137], v[82:97]
	ds_read_b128 v[170:173], v176 offset:49152
	ds_read_b128 v[180:183], v176 offset:50176
	ds_read_b128 v[184:187], v176 offset:51200
	ds_read_b128 v[208:211], v176 offset:52224
	v_mfma_f32_32x32x16_bf16 v[66:81], v[188:191], v[134:137], v[66:81]
	v_mfma_f32_32x32x16_bf16 v[114:129], v[192:195], v[138:141], v[114:129]
	v_mfma_f32_32x32x16_bf16 v[98:113], v[196:199], v[138:141], v[98:113]
	ds_read_b128 v[134:137], v176 offset:53248
	ds_read_b128 v[188:191], v176 offset:54272
	ds_read_b128 v[192:195], v176 offset:55296
	ds_read_b128 v[196:199], v176 offset:56320
	v_mfma_f32_32x32x16_bf16 v[82:97], v[200:203], v[138:141], v[82:97]
	v_mfma_f32_32x32x16_bf16 v[66:81], v[204:207], v[138:141], v[66:81]
	s_waitcnt lgkmcnt(0)
	v_mfma_f32_32x32x16_bf16 v[114:129], v[170:173], v[142:145], v[114:129]
	v_mfma_f32_32x32x16_bf16 v[98:113], v[180:183], v[142:145], v[98:113]
	v_mfma_f32_32x32x16_bf16 v[82:97], v[184:187], v[142:145], v[82:97]
	v_mfma_f32_32x32x16_bf16 v[66:81], v[208:211], v[142:145], v[66:81]
	v_mfma_f32_32x32x16_bf16 v[114:129], v[134:137], v[146:149], v[114:129]
	s_waitcnt vmcnt(0) lgkmcnt(0)
	s_barrier
	v_mfma_f32_32x32x16_bf16 v[98:113], v[188:191], v[146:149], v[98:113]
	v_mfma_f32_32x32x16_bf16 v[82:97], v[192:195], v[146:149], v[82:97]
	ds_read_b128 v[134:137], v176
	ds_read_b128 v[138:141], v176 offset:1024
	ds_read_b128 v[142:145], v176 offset:2048
	ds_read_b128 v[170:173], v176 offset:3072
	ds_read_b128 v[180:183], v176 offset:4096
	ds_read_b128 v[184:187], v176 offset:5120
	ds_read_b128 v[188:191], v176 offset:6144
	ds_read_b128 v[192:195], v176 offset:7168
	v_mfma_f32_32x32x16_bf16 v[66:81], v[196:199], v[146:149], v[66:81]
	s_waitcnt lgkmcnt(5)
	v_mfma_f32_32x32x16_bf16 v[82:97], v[142:145], v[150:153], v[82:97]
	ds_read_b128 v[142:145], v176 offset:8192
	ds_read_b128 v[146:149], v176 offset:9216
	ds_read_b128 v[196:199], v176 offset:10240
	ds_read_b128 v[200:203], v176 offset:11264
	v_mfma_f32_32x32x16_bf16 v[114:129], v[134:137], v[150:153], v[114:129]
	v_mfma_f32_32x32x16_bf16 v[98:113], v[138:141], v[150:153], v[98:113]
	s_waitcnt lgkmcnt(8)
	v_mfma_f32_32x32x16_bf16 v[66:81], v[170:173], v[150:153], v[66:81]
	ds_read_b128 v[150:153], v176 offset:12288
	ds_read_b128 v[170:173], v176 offset:13312
	ds_read_b128 v[138:141], v176 offset:14336
	ds_read_b128 v[134:137], v176 offset:15360
	s_waitcnt lgkmcnt(11)
	v_mfma_f32_32x32x16_bf16 v[114:129], v[180:183], v[156:159], v[114:129]
	s_waitcnt lgkmcnt(10)
	v_mfma_f32_32x32x16_bf16 v[98:113], v[184:187], v[156:159], v[98:113]
	s_waitcnt lgkmcnt(9)
	v_mfma_f32_32x32x16_bf16 v[82:97], v[188:191], v[156:159], v[82:97]
	s_waitcnt lgkmcnt(8)
	v_mfma_f32_32x32x16_bf16 v[66:81], v[192:195], v[156:159], v[66:81]
	s_waitcnt lgkmcnt(7)
	v_mfma_f32_32x32x16_bf16 v[114:129], v[142:145], v[166:169], v[114:129]
	s_waitcnt lgkmcnt(6)
	v_mfma_f32_32x32x16_bf16 v[98:113], v[146:149], v[166:169], v[98:113]
	s_waitcnt lgkmcnt(5)
	v_mfma_f32_32x32x16_bf16 v[82:97], v[196:199], v[166:169], v[82:97]
	s_waitcnt lgkmcnt(4)
	v_mfma_f32_32x32x16_bf16 v[66:81], v[200:203], v[166:169], v[66:81]
	s_waitcnt lgkmcnt(3)
	v_mfma_f32_32x32x16_bf16 v[114:129], v[150:153], v[130:133], v[114:129]
	v_and_b32_e32 v0, 7, v0
	v_lshlrev_b32_e32 v174, 4, v0
	v_or_b32_e32 v144, v1, v174
	v_mad_u32_u24 v145, v161, s1, v144
	v_lshl_add_u64 v[142:143], s[6:7], 0, v[178:179]
	s_nop 6
	v_mul_f32_e32 v0, 0x3c23d70a, v114
	v_max_f32_e32 v0, v114, v0
	v_mul_f32_e32 v1, 0x3c23d70a, v115
	v_max_f32_e32 v1, v115, v1
	v_pk_add_f32 v[50:51], v[50:51], v[0:1]
	v_mul_f32_e32 v0, 0x3c23d70a, v116
	v_max_f32_e32 v0, v116, v0
	v_mul_f32_e32 v1, 0x3c23d70a, v117
	v_max_f32_e32 v114, v117, v117
	v_max_f32_e32 v1, v114, v1
	v_pk_add_f32 v[52:53], v[52:53], v[0:1]
	v_mul_f32_e32 v0, 0x3c23d70a, v118
	ds_write_b128 v160, v[50:53] offset:61440
	v_max_f32_e32 v0, v118, v0
	v_mul_f32_e32 v1, 0x3c23d70a, v119
	v_max_f32_e32 v1, v119, v1
	v_pk_add_f32 v[50:51], v[54:55], v[0:1]
	v_mul_f32_e32 v0, 0x3c23d70a, v120
	v_max_f32_e32 v0, v120, v0
	v_mul_f32_e32 v1, 0x3c23d70a, v121
	v_max_f32_e32 v1, v121, v1
	v_pk_add_f32 v[52:53], v[56:57], v[0:1]
	v_mul_f32_e32 v0, 0x3c23d70a, v122
	ds_write_b128 v160, v[50:53] offset:61472
	v_max_f32_e32 v0, v122, v0
	v_mul_f32_e32 v1, 0x3c23d70a, v123
	v_max_f32_e32 v1, v123, v1
	v_pk_add_f32 v[50:51], v[58:59], v[0:1]
	v_mul_f32_e32 v0, 0x3c23d70a, v124
	v_max_f32_e32 v0, v124, v0
	v_mul_f32_e32 v1, 0x3c23d70a, v125
	v_max_f32_e32 v1, v125, v1
	v_pk_add_f32 v[52:53], v[60:61], v[0:1]
	v_mul_f32_e32 v0, 0x3c23d70a, v126
	ds_write_b128 v160, v[50:53] offset:61504
	v_max_f32_e32 v0, v126, v0
	v_mul_f32_e32 v1, 0x3c23d70a, v127
	v_max_f32_e32 v1, v127, v1
	v_pk_add_f32 v[50:51], v[62:63], v[0:1]
	v_mul_f32_e32 v0, 0x3c23d70a, v128
	v_max_f32_e32 v0, v128, v0
	v_mul_f32_e32 v1, 0x3c23d70a, v129
	v_max_f32_e32 v1, v129, v1
	v_pk_add_f32 v[52:53], v[64:65], v[0:1]
	ds_write_b128 v160, v[50:53] offset:61536
	ds_read_b128 v[50:53], v145 offset:61440
	v_add_u32_e32 v62, v144, v165
	ds_read_b128 v[54:57], v62 offset:61440
	v_lshl_add_u64 v[142:143], v[142:143], 0, v[174:175]
	v_lshlrev_b32_e32 v174, 9, v161
	s_waitcnt lgkmcnt(8)
	v_mfma_f32_32x32x16_bf16 v[98:113], v[170:173], v[130:133], v[98:113]
	v_lshl_add_u64 v[0:1], v[142:143], 0, v[174:175]
	s_waitcnt lgkmcnt(1)
	global_store_dwordx4 v[0:1], v[50:53], off sc1
	v_add_u32_e32 v63, v144, v164
	v_add_u32_e32 v64, v144, v163
	v_or_b32_e32 v50, 0x1000, v174
	v_mov_b32_e32 v51, v175
	v_lshl_add_u64 v[50:51], v[142:143], 0, v[50:51]
	ds_read_b128 v[58:61], v64 offset:61440
	s_waitcnt lgkmcnt(1)
	global_store_dwordx4 v[50:51], v[54:57], off sc1
	ds_read_b128 v[54:57], v63 offset:61440
	v_or_b32_e32 v52, 0x2000, v174
	v_mov_b32_e32 v53, v175
	v_lshl_add_u64 v[52:53], v[142:143], 0, v[52:53]
	v_or_b32_e32 v174, 0x3000, v174
	s_waitcnt lgkmcnt(0)
	global_store_dwordx4 v[52:53], v[54:57], off sc1
	v_mfma_f32_32x32x16_bf16 v[82:97], v[138:141], v[130:133], v[82:97]
	s_nop 0
	v_lshl_add_u64 v[54:55], v[142:143], 0, v[174:175]
	v_mul_f32_e32 v56, 0x3c23d70a, v98
	global_store_dwordx4 v[54:55], v[58:61], off sc1
	v_max_f32_e32 v56, v98, v56
	v_mul_f32_e32 v57, 0x3c23d70a, v99
	v_max_f32_e32 v57, v99, v57
	v_pk_add_f32 v[34:35], v[34:35], v[56:57]
	v_mul_f32_e32 v56, 0x3c23d70a, v100
	v_max_f32_e32 v56, v100, v56
	v_mul_f32_e32 v57, 0x3c23d70a, v101
	v_max_f32_e32 v58, v101, v101
	v_max_f32_e32 v57, v58, v57
	v_pk_add_f32 v[36:37], v[36:37], v[56:57]
	ds_write_b128 v160, v[34:37] offset:61440
	v_mul_f32_e32 v34, 0x3c23d70a, v102
	v_max_f32_e32 v34, v102, v34
	v_mul_f32_e32 v35, 0x3c23d70a, v103
	v_max_f32_e32 v35, v103, v35
	v_mul_f32_e32 v36, 0x3c23d70a, v104
	v_pk_add_f32 v[34:35], v[38:39], v[34:35]
	v_max_f32_e32 v36, v104, v36
	v_mul_f32_e32 v37, 0x3c23d70a, v105
	v_max_f32_e32 v37, v105, v37
	v_pk_add_f32 v[36:37], v[40:41], v[36:37]
	ds_write_b128 v160, v[34:37] offset:61472
	v_mul_f32_e32 v34, 0x3c23d70a, v106
	v_max_f32_e32 v34, v106, v34
	v_mul_f32_e32 v35, 0x3c23d70a, v107
	v_max_f32_e32 v35, v107, v35
	v_mul_f32_e32 v36, 0x3c23d70a, v108
	v_max_f32_e32 v36, v108, v36
	v_mul_f32_e32 v37, 0x3c23d70a, v109
	v_max_f32_e32 v37, v109, v37
	v_pk_add_f32 v[34:35], v[42:43], v[34:35]
	v_pk_add_f32 v[36:37], v[44:45], v[36:37]
	ds_write_b128 v160, v[34:37] offset:61504
	v_mul_f32_e32 v34, 0x3c23d70a, v110
	v_max_f32_e32 v34, v110, v34
	v_mul_f32_e32 v35, 0x3c23d70a, v111
	v_max_f32_e32 v35, v111, v35
	v_mul_f32_e32 v36, 0x3c23d70a, v112
	v_max_f32_e32 v36, v112, v36
	v_mul_f32_e32 v37, 0x3c23d70a, v113
	v_max_f32_e32 v37, v113, v37
	v_pk_add_f32 v[34:35], v[46:47], v[34:35]
	v_pk_add_f32 v[36:37], v[48:49], v[36:37]
	ds_write_b128 v160, v[34:37] offset:61536
	ds_read_b128 v[34:37], v145 offset:61440
	ds_read_b128 v[38:41], v62 offset:61440
	ds_read_b128 v[42:45], v63 offset:61440
	ds_read_b128 v[46:49], v64 offset:61440
	s_waitcnt lgkmcnt(3)
	global_store_dwordx4 v[0:1], v[34:37], off offset:128 sc1
	s_waitcnt lgkmcnt(2)
	global_store_dwordx4 v[50:51], v[38:41], off offset:128 sc1
	s_waitcnt lgkmcnt(1)
	global_store_dwordx4 v[52:53], v[42:45], off offset:128 sc1
	s_waitcnt lgkmcnt(0)
	global_store_dwordx4 v[54:55], v[46:49], off offset:128 sc1
	v_mul_f32_e32 v34, 0x3c23d70a, v82
	v_max_f32_e32 v34, v82, v34
	v_mul_f32_e32 v35, 0x3c23d70a, v83
	v_max_f32_e32 v35, v83, v35
	v_pk_add_f32 v[18:19], v[18:19], v[34:35]
	v_mul_f32_e32 v34, 0x3c23d70a, v84
	v_max_f32_e32 v34, v84, v34
	v_mul_f32_e32 v35, 0x3c23d70a, v85
	v_max_f32_e32 v36, v85, v85
	v_max_f32_e32 v35, v36, v35
	v_pk_add_f32 v[20:21], v[20:21], v[34:35]
	ds_write_b128 v160, v[18:21] offset:61440
	v_mul_f32_e32 v18, 0x3c23d70a, v86
	v_max_f32_e32 v18, v86, v18
	v_mul_f32_e32 v19, 0x3c23d70a, v87
	v_max_f32_e32 v19, v87, v19
	v_mul_f32_e32 v20, 0x3c23d70a, v88
	v_pk_add_f32 v[18:19], v[22:23], v[18:19]
	v_max_f32_e32 v20, v88, v20
	v_mul_f32_e32 v21, 0x3c23d70a, v89
	v_max_f32_e32 v21, v89, v21
	v_pk_add_f32 v[20:21], v[24:25], v[20:21]
	ds_write_b128 v160, v[18:21] offset:61472
	v_mul_f32_e32 v18, 0x3c23d70a, v90
	v_max_f32_e32 v18, v90, v18
	v_mul_f32_e32 v19, 0x3c23d70a, v91
	v_max_f32_e32 v19, v91, v19
	v_mul_f32_e32 v20, 0x3c23d70a, v92
	v_max_f32_e32 v20, v92, v20
	v_mul_f32_e32 v21, 0x3c23d70a, v93
	v_max_f32_e32 v21, v93, v21
	v_pk_add_f32 v[18:19], v[26:27], v[18:19]
	v_pk_add_f32 v[20:21], v[28:29], v[20:21]
	ds_write_b128 v160, v[18:21] offset:61504
	v_mul_f32_e32 v18, 0x3c23d70a, v94
	v_max_f32_e32 v18, v94, v18
	v_mul_f32_e32 v19, 0x3c23d70a, v95
	v_max_f32_e32 v19, v95, v19
	v_mul_f32_e32 v20, 0x3c23d70a, v96
	v_max_f32_e32 v20, v96, v20
	v_mul_f32_e32 v21, 0x3c23d70a, v97
	v_mfma_f32_32x32x16_bf16 v[66:81], v[134:137], v[130:133], v[66:81]
	v_max_f32_e32 v21, v97, v21
	v_add_f32_e64 v18, v30, v18
	v_add_f32_e64 v19, v31, v19
	v_add_f32_e64 v20, v32, v20
	v_add_f32_e64 v21, v33, v21
	ds_write_b128 v160, v[18:21] offset:61536
	ds_read_b128 v[18:21], v145 offset:61440
	ds_read_b128 v[22:25], v62 offset:61440
	ds_read_b128 v[26:29], v63 offset:61440
	ds_read_b128 v[30:33], v64 offset:61440
	s_waitcnt lgkmcnt(3)
	global_store_dwordx4 v[0:1], v[18:21], off offset:256 sc1
	s_waitcnt lgkmcnt(2)
	global_store_dwordx4 v[50:51], v[22:25], off offset:256 sc1
	s_waitcnt lgkmcnt(1)
	global_store_dwordx4 v[52:53], v[26:29], off offset:256 sc1
	s_waitcnt lgkmcnt(0)
	global_store_dwordx4 v[54:55], v[30:33], off offset:256 sc1
	v_mul_f32_e32 v18, 0x3c23d70a, v66
	v_max_f32_e32 v18, v66, v18
	v_mul_f32_e32 v19, 0x3c23d70a, v67
	v_max_f32_e32 v19, v67, v19
	v_pk_add_f32 v[2:3], v[2:3], v[18:19]
	v_mul_f32_e32 v18, 0x3c23d70a, v68
	v_max_f32_e32 v18, v68, v18
	v_mul_f32_e32 v19, 0x3c23d70a, v69
	v_max_f32_e32 v20, v69, v69
	v_max_f32_e32 v19, v20, v19
	v_pk_add_f32 v[4:5], v[4:5], v[18:19]
	ds_write_b128 v160, v[2:5] offset:61440
	v_mul_f32_e32 v2, 0x3c23d70a, v70
	v_max_f32_e32 v2, v70, v2
	v_mul_f32_e32 v3, 0x3c23d70a, v71
	v_max_f32_e32 v3, v71, v3
	v_mul_f32_e32 v4, 0x3c23d70a, v72
	v_pk_add_f32 v[2:3], v[6:7], v[2:3]
	v_max_f32_e32 v4, v72, v4
	v_mul_f32_e32 v5, 0x3c23d70a, v73
	v_max_f32_e32 v5, v73, v5
	v_pk_add_f32 v[4:5], v[8:9], v[4:5]
	ds_write_b128 v160, v[2:5] offset:61472
	v_mul_f32_e32 v2, 0x3c23d70a, v74
	v_max_f32_e32 v2, v74, v2
	v_mul_f32_e32 v3, 0x3c23d70a, v75
	v_max_f32_e32 v3, v75, v3
	v_mul_f32_e32 v4, 0x3c23d70a, v76
	v_max_f32_e32 v4, v76, v4
	v_mul_f32_e32 v5, 0x3c23d70a, v77
	v_max_f32_e32 v5, v77, v5
	v_pk_add_f32 v[2:3], v[10:11], v[2:3]
	v_pk_add_f32 v[4:5], v[12:13], v[4:5]
	ds_write_b128 v160, v[2:5] offset:61504
	v_mul_f32_e32 v2, 0x3c23d70a, v78
	v_max_f32_e32 v2, v78, v2
	v_mul_f32_e32 v3, 0x3c23d70a, v79
	v_max_f32_e32 v3, v79, v3
	v_mul_f32_e32 v4, 0x3c23d70a, v80
	v_max_f32_e32 v4, v80, v4
	v_mul_f32_e32 v5, 0x3c23d70a, v81
	v_max_f32_e32 v5, v81, v5
	v_pk_add_f32 v[2:3], v[14:15], v[2:3]
	v_pk_add_f32 v[4:5], v[16:17], v[4:5]
	ds_write_b128 v160, v[2:5] offset:61536
	ds_read_b128 v[2:5], v145 offset:61440
	ds_read_b128 v[6:9], v62 offset:61440
	ds_read_b128 v[10:13], v63 offset:61440
	ds_read_b128 v[14:17], v64 offset:61440
	s_waitcnt lgkmcnt(3)
	global_store_dwordx4 v[0:1], v[2:5], off offset:384 sc1
	s_waitcnt lgkmcnt(2)
	global_store_dwordx4 v[50:51], v[6:9], off offset:384 sc1
	s_waitcnt lgkmcnt(1)
	global_store_dwordx4 v[52:53], v[10:13], off offset:384 sc1
	s_waitcnt lgkmcnt(0)
	global_store_dwordx4 v[54:55], v[14:17], off offset:384 sc1
	s_endpgm
